# attention loops: row-sum adds spread behind their cvt only (original waits and MFMA order)
# speedup vs baseline: 1.0034x; 1.0034x over previous
.LBB0_926:
	v_lshlrev_b32_e32 v12, 10, v4
	v_and_b32_e32 v4, 19, v3
	v_lshlrev_b32_e32 v5, 1, v2
	v_lshrrev_b32_e32 v3, 1, v3
	s_add_u32 s12, s30, s25
	v_and_b32_e32 v5, 8, v5
	v_and_b32_e32 v3, 4, v3
	s_addc_u32 s13, s31, s26
	v_or3_b32 v3, v4, v5, v3
	v_lshl_add_u64 v[4:5], s[12:13], 0, v[0:1]
	v_lshl_add_u64 v[4:5], v[4:5], 0, s[52:53]
	s_add_i32 m0, s27, 0x8000
	v_lshl_or_b32 v231, v3, 4, v12
	global_load_lds_dwordx4 v[4:5], off
	v_mov_b32_e32 v178, v1
	v_add_u32_e32 v232, 0, v231
	s_waitcnt vmcnt(0)
	s_waitcnt vmcnt(0) lgkmcnt(0)
	s_barrier
	ds_read_b128 v[4:7], v232
	ds_read_b128 v[98:101], v232 offset:512
	s_waitcnt lgkmcnt(1)
	v_mfma_f32_32x32x16_bf16 v[82:97], v[4:7], v[130:133], 0
	v_lshl_or_b32 v233, v2, 4, v12
	v_mov_b32_e32 v2, 0
	s_mov_b32 s12, 1
	s_mov_b32 s33, 0
	v_add_u32_e32 v234, 0, v233
	s_mov_b32 s13, 2
	s_mov_b32 s30, 0
	v_mfma_f32_32x32x16_bf16 v[66:81], v[4:7], v[170:173], 0
	ds_read_b128 v[4:7], v232 offset:2048
	ds_read_b128 v[194:197], v232 offset:2560
	ds_read_b128 v[8:11], v232 offset:4096
	ds_read_b128 v[12:15], v232 offset:6144
	ds_read_b128 v[18:21], v232 offset:8192
	ds_read_b128 v[22:25], v232 offset:10240
	s_mov_b32 s31, 0
	v_mov_b32_e32 v179, v178
	v_mov_b32_e32 v180, v178
	v_mov_b32_e32 v181, v178
	s_waitcnt lgkmcnt(5)
	v_mfma_f32_32x32x16_bf16 v[82:97], v[4:7], v[134:137], v[82:97]
	v_mov_b32_e32 v182, v178
	v_mov_b32_e32 v183, v178
	v_mov_b32_e32 v184, v178
	v_mov_b32_e32 v185, v178
	v_mov_b32_e32 v190, v178
	v_mov_b32_e32 v191, v178
	v_mov_b32_e32 v192, v178
	v_mfma_f32_32x32x16_bf16 v[66:81], v[4:7], v[138:141], v[66:81]
	v_mov_b32_e32 v193, v178
	v_mov_b32_e32 v186, v178
	v_mov_b32_e32 v187, v178
	v_mov_b32_e32 v188, v178
	v_mov_b32_e32 v189, v178
	v_mov_b32_e32 v3, v2
	v_mov_b32_e32 v4, v2
	s_waitcnt lgkmcnt(3)
	v_mfma_f32_32x32x16_bf16 v[82:97], v[8:11], v[146:149], v[82:97]
	v_mov_b32_e32 v5, v2
	v_mov_b32_e32 v6, v2
	v_mov_b32_e32 v7, v2
	v_mov_b32_e32 v16, v2
	v_mov_b32_e32 v17, v2
	v_mov_b32_e32 v50, v2
	v_mov_b32_e32 v51, v2
	v_mfma_f32_32x32x16_bf16 v[66:81], v[8:11], v[142:145], v[66:81]
	v_mov_b32_e32 v8, v2
	v_mov_b32_e32 v9, v2
	v_mov_b32_e32 v10, v2
	v_mov_b32_e32 v11, v2
	v_mov_b32_e32 v52, v2
	v_mov_b32_e32 v53, v2
	v_mov_b32_e32 v54, v2
	s_waitcnt lgkmcnt(2)
	v_mfma_f32_32x32x16_bf16 v[82:97], v[12:15], v[150:153], v[82:97]
	v_mov_b32_e32 v55, v2
	v_mov_b32_e32 v56, v2
	v_mov_b32_e32 v57, v2
	v_mov_b32_e32 v58, v2
	v_mov_b32_e32 v59, v2
	v_mov_b32_e32 v60, v2
	v_mov_b32_e32 v61, v2
	v_mfma_f32_32x32x16_bf16 v[66:81], v[12:15], v[154:157], v[66:81]
	v_mov_b32_e32 v12, v2
	v_mov_b32_e32 v13, v2
	v_mov_b32_e32 v14, v2
	v_mov_b32_e32 v15, v2
	v_mov_b32_e32 v62, v2
	v_mov_b32_e32 v63, v2
	v_mov_b32_e32 v64, v2
	s_waitcnt lgkmcnt(1)
	v_mfma_f32_32x32x16_bf16 v[82:97], v[18:21], v[162:165], v[82:97]
	v_mov_b32_e32 v65, v2
	v_mov_b32_e32 v34, v2
	v_mov_b32_e32 v35, v2
	v_mov_b32_e32 v36, v2
	v_mov_b32_e32 v37, v2
	v_mov_b32_e32 v38, v2
	v_mov_b32_e32 v39, v2
	v_mfma_f32_32x32x16_bf16 v[66:81], v[18:21], v[158:161], v[66:81]
	v_mov_b32_e32 v40, v2
	v_mov_b32_e32 v41, v2
	v_mov_b32_e32 v42, v2
	v_mov_b32_e32 v43, v2
	v_mov_b32_e32 v44, v2
	v_mov_b32_e32 v45, v2
	v_mov_b32_e32 v46, v2
	s_waitcnt lgkmcnt(0)
	v_mfma_f32_32x32x16_bf16 v[82:97], v[22:25], v[166:169], v[82:97]
	v_mov_b32_e32 v47, v2
	v_mov_b32_e32 v48, v2
	v_mov_b32_e32 v49, v2
	v_mov_b32_e32 v18, v2
	v_mov_b32_e32 v19, v2
	v_mov_b32_e32 v20, v2
	v_mov_b32_e32 v21, v2
	v_mfma_f32_32x32x16_bf16 v[66:81], v[22:25], v[174:177], v[66:81]
	v_mov_b32_e32 v22, v2
	v_mov_b32_e32 v23, v2
	v_mov_b32_e32 v24, v2
	v_mov_b32_e32 v25, v2
	v_mov_b32_e32 v26, v2
	v_mov_b32_e32 v27, v2
	v_mov_b32_e32 v28, v2
	v_mov_b32_e32 v29, v2
	v_mov_b32_e32 v30, v2
	v_mov_b32_e32 v31, v2
	v_mov_b32_e32 v32, v2
	v_mov_b32_e32 v33, v2
	v_mov_b32_e32 v202, v2
	v_mov_b32_e32 v203, v2
	v_mov_b32_e32 v212, v202
	v_mov_b32_e32 v213, v203

.LBB0_929:
	s_lshl_b64 s[38:39], s[88:89], 13
	v_lshl_add_u64 v[102:103], v[214:215], 0, s[38:39]
	s_add_i32 m0, s34, 0x3000
	s_mul_i32 s34, s30, 0x5000
	global_load_lds_dwordx4 v[102:103], off
	s_add_i32 s34, s34, 0
	v_add_u32_e32 v208, s34, v231
	ds_read_b128 v[204:207], v208 offset:4608
	v_exp_f32_e32 v82, v82
	v_exp_f32_e32 v83, v83
	s_mul_i32 s35, s12, 0x5000
	s_mulk_i32 s33, 0x5000
	v_add_u32_e32 v235, s34, v233
	v_add_u32_e32 v210, s35, v232
	v_add_u32_e32 v209, s33, v234
	v_mfma_f32_32x32x16_bf16 v[114:129], v[98:101], v[130:133], 0
	v_mfma_f32_32x32x16_bf16 v[98:113], v[98:101], v[170:173], 0
	v_cvt_pk_bf16_f32 v198, v82, v83
	v_add_f32_e32 v212, v82, v212
	v_add_f32_e32 v212, v83, v212
	v_exp_f32_e32 v200, v84
	v_exp_f32_e32 v201, v85
	ds_read_b128 v[82:85], v208 offset:6656
	v_exp_f32_e32 v86, v86
	v_exp_f32_e32 v87, v87
	v_cvt_pk_bf16_f32 v199, v200, v201
	v_add_f32_e32 v212, v200, v212
	v_add_f32_e32 v212, v201, v212
	v_mfma_f32_32x32x16_bf16 v[114:129], v[194:197], v[134:137], v[114:129]
	v_mfma_f32_32x32x16_bf16 v[98:113], v[194:197], v[138:141], v[98:113]
	v_exp_f32_e32 v195, v88
	v_exp_f32_e32 v196, v89
	v_cvt_pk_bf16_f32 v200, v86, v87
	v_add_f32_e32 v212, v86, v212
	v_add_f32_e32 v212, v87, v212
	ds_read_b128 v[86:89], v208 offset:8704
	v_cvt_pk_bf16_f32 v201, v195, v196
	v_add_f32_e32 v212, v195, v212
	v_add_f32_e32 v212, v196, v212
	s_waitcnt lgkmcnt(0)
	v_mfma_f32_32x32x16_bf16 v[114:129], v[204:207], v[146:149], v[114:129]
	v_mfma_f32_32x32x16_bf16 v[98:113], v[204:207], v[142:145], v[98:113]
	v_exp_f32_e32 v90, v90
	v_exp_f32_e32 v91, v91
	ds_read_b128 v[204:207], v208 offset:10752
	v_cvt_pk_bf16_f32 v194, v90, v91
	v_add_f32_e32 v212, v90, v212
	v_add_f32_e32 v212, v91, v212
	v_exp_f32_e32 v90, v92
	v_exp_f32_e32 v91, v93
	v_mfma_f32_32x32x16_bf16 v[114:129], v[82:85], v[150:153], v[114:129]
	v_mfma_f32_32x32x16_bf16 v[98:113], v[82:85], v[154:157], v[98:113]
	v_cvt_pk_bf16_f32 v195, v90, v91
	v_add_f32_e32 v212, v90, v212
	v_add_f32_e32 v212, v91, v212
	v_exp_f32_e32 v90, v94
	v_exp_f32_e32 v91, v95
	ds_read_b128 v[82:85], v209 offset:16384
	v_exp_f32_e32 v95, v96
	v_exp_f32_e32 v96, v97
	v_cvt_pk_bf16_f32 v196, v90, v91
	v_add_f32_e32 v212, v90, v212
	v_add_f32_e32 v212, v91, v212
	v_mfma_f32_32x32x16_bf16 v[114:129], v[86:89], v[162:165], v[114:129]
	v_mfma_f32_32x32x16_bf16 v[98:113], v[86:89], v[158:161], v[98:113]
	ds_read_b128 v[90:93], v209 offset:16896
	v_cvt_pk_bf16_f32 v197, v95, v96
	v_add_f32_e32 v212, v95, v212
	v_add_f32_e32 v212, v96, v212
	v_exp_f32_e32 v66, v66
	v_exp_f32_e32 v67, v67
	s_waitcnt lgkmcnt(0)
	v_mfma_f32_32x32x16_bf16 v[114:129], v[204:207], v[166:169], v[114:129]
	v_mfma_f32_32x32x16_bf16 v[98:113], v[204:207], v[174:177], v[98:113]
	v_exp_f32_e32 v87, v68
	v_exp_f32_e32 v88, v69
	v_cvt_pk_bf16_f32 v202, v66, v67
	v_add_f32_e32 v213, v66, v213
	v_add_f32_e32 v213, v67, v213
	v_mfma_f32_32x32x16_bf16 v[18:33], v[82:85], v[178:181], v[18:33]
	ds_read_b128 v[66:69], v209 offset:18432
	v_exp_f32_e32 v70, v70
	v_exp_f32_e32 v71, v71
	v_cvt_pk_bf16_f32 v203, v87, v88
	v_add_f32_e32 v213, v87, v213
	v_add_f32_e32 v213, v88, v213
	v_mfma_f32_32x32x16_bf16 v[34:49], v[90:93], v[178:181], v[34:49]
	ds_read_b128 v[86:89], v209 offset:18944
	v_cvt_pk_bf16_f32 v204, v70, v71
	v_add_f32_e32 v213, v70, v213
	v_add_f32_e32 v213, v71, v213
	v_exp_f32_e32 v70, v72
	v_exp_f32_e32 v71, v73
	v_mfma_f32_32x32x16_bf16 v[50:65], v[82:85], v[190:193], v[50:65]
	v_cvt_pk_bf16_f32 v205, v70, v71
	v_add_f32_e32 v213, v70, v213
	v_add_f32_e32 v213, v71, v213
	v_mfma_f32_32x32x16_bf16 v[2:17], v[90:93], v[190:193], v[2:17]
	v_exp_f32_e32 v74, v74
	v_exp_f32_e32 v75, v75
	s_waitcnt lgkmcnt(0)
	v_mfma_f32_32x32x16_bf16 v[18:33], v[66:69], v[182:185], v[18:33]
	ds_read_b128 v[70:73], v210
	v_cvt_pk_bf16_f32 v206, v74, v75
	v_add_f32_e32 v213, v74, v213
	v_add_f32_e32 v213, v75, v213
	v_exp_f32_e32 v74, v76
	v_exp_f32_e32 v75, v77
	v_mfma_f32_32x32x16_bf16 v[34:49], v[86:89], v[182:185], v[34:49]
	v_cvt_pk_bf16_f32 v207, v74, v75
	v_add_f32_e32 v213, v74, v213
	v_add_f32_e32 v213, v75, v213
	v_exp_f32_e32 v74, v78
	v_exp_f32_e32 v75, v79
	v_mfma_f32_32x32x16_bf16 v[50:65], v[66:69], v[186:189], v[50:65]
	ds_read_b128 v[180:183], v210 offset:2048
	v_exp_f32_e32 v67, v80
	v_exp_f32_e32 v68, v81
	v_cvt_pk_bf16_f32 v208, v74, v75
	v_add_f32_e32 v213, v74, v213
	v_add_f32_e32 v213, v75, v213
	v_mfma_f32_32x32x16_bf16 v[2:17], v[86:89], v[186:189], v[2:17]
	v_cvt_pk_bf16_f32 v209, v67, v68
	v_add_f32_e32 v213, v67, v213
	v_add_f32_e32 v213, v68, v213
	s_waitcnt lgkmcnt(0)
	v_mfma_f32_32x32x16_bf16 v[82:97], v[70:73], v[130:133], 0
	ds_read_b128 v[184:187], v210 offset:4096
	v_exp_f32_e32 v114, v114
	v_exp_f32_e32 v115, v115
	v_mfma_f32_32x32x16_bf16 v[66:81], v[70:73], v[170:173], 0
	v_exp_f32_e32 v188, v116
	v_exp_f32_e32 v189, v117
	v_cvt_pk_bf16_f32 v178, v114, v115
	v_add_f32_e32 v212, v114, v212
	v_add_f32_e32 v212, v115, v212
	v_mfma_f32_32x32x16_bf16 v[82:97], v[180:183], v[134:137], v[82:97]
	ds_read_b128 v[114:117], v210 offset:6144
	v_cvt_pk_bf16_f32 v179, v188, v189
	v_add_f32_e32 v212, v188, v212
	v_add_f32_e32 v212, v189, v212
	v_exp_f32_e32 v118, v118
	v_exp_f32_e32 v236, v119
	v_mfma_f32_32x32x16_bf16 v[66:81], v[180:183], v[138:141], v[66:81]
	v_cvt_pk_bf16_f32 v180, v118, v236
	v_add_f32_e32 v212, v118, v212
	v_add_f32_e32 v212, v236, v212
	v_exp_f32_e32 v240, v120
	v_exp_f32_e32 v242, v121
	s_waitcnt lgkmcnt(0)
	v_mfma_f32_32x32x16_bf16 v[82:97], v[184:187], v[146:149], v[82:97]
	ds_read_b128 v[118:121], v210 offset:8192
	v_cvt_pk_bf16_f32 v181, v240, v242
	v_add_f32_e32 v212, v240, v212
	v_add_f32_e32 v212, v242, v212
	v_mfma_f32_32x32x16_bf16 v[66:81], v[184:187], v[142:145], v[66:81]
	v_exp_f32_e32 v244, v122
	v_exp_f32_e32 v246, v123
	v_mfma_f32_32x32x16_bf16 v[82:97], v[114:117], v[150:153], v[82:97]
	ds_read_b128 v[186:189], v210 offset:10240
	v_cvt_pk_bf16_f32 v182, v244, v246
	v_add_f32_e32 v212, v244, v212
	v_add_f32_e32 v212, v246, v212
	v_exp_f32_e32 v248, v124
	v_exp_f32_e32 v216, v125
	v_mfma_f32_32x32x16_bf16 v[66:81], v[114:117], v[154:157], v[66:81]
	v_cvt_pk_bf16_f32 v183, v248, v216
	v_add_f32_e32 v212, v248, v212
	v_add_f32_e32 v212, v216, v212
	v_exp_f32_e32 v218, v126
	v_exp_f32_e32 v220, v127
	s_waitcnt lgkmcnt(0)
	v_mfma_f32_32x32x16_bf16 v[82:97], v[118:121], v[162:165], v[82:97]
	ds_read_b128 v[114:117], v235 offset:12288
	v_cvt_pk_bf16_f32 v184, v218, v220
	v_add_f32_e32 v212, v218, v212
	v_add_f32_e32 v212, v220, v212
	v_exp_f32_e32 v222, v128
	v_exp_f32_e32 v224, v129
	v_mfma_f32_32x32x16_bf16 v[66:81], v[118:121], v[158:161], v[66:81]
	ds_read_b128 v[122:125], v235 offset:12800
	v_cvt_pk_bf16_f32 v185, v222, v224
	v_add_f32_e32 v212, v222, v212
	v_add_f32_e32 v212, v224, v212
	v_mfma_f32_32x32x16_bf16 v[82:97], v[186:189], v[166:169], v[82:97]
	v_exp_f32_e32 v98, v98
	v_exp_f32_e32 v99, v99
	v_mfma_f32_32x32x16_bf16 v[66:81], v[186:189], v[174:177], v[66:81]
	v_cvt_pk_bf16_f32 v190, v98, v99
	v_add_f32_e32 v213, v98, v213
	v_add_f32_e32 v213, v99, v213
	v_exp_f32_e32 v98, v100
	v_exp_f32_e32 v99, v101
	s_waitcnt lgkmcnt(0)
	v_mfma_f32_32x32x16_bf16 v[18:33], v[114:117], v[198:201], v[18:33]
	ds_read_b128 v[118:121], v235 offset:14336
	v_cvt_pk_bf16_f32 v191, v98, v99
	v_add_f32_e32 v213, v98, v213
	v_add_f32_e32 v213, v99, v213
	v_exp_f32_e32 v98, v102
	v_exp_f32_e32 v237, v103
	v_mfma_f32_32x32x16_bf16 v[34:49], v[122:125], v[198:201], v[34:49]
	ds_read_b128 v[126:129], v235 offset:14848
	v_cvt_pk_bf16_f32 v192, v98, v237
	v_add_f32_e32 v213, v98, v213
	v_add_f32_e32 v213, v237, v213
	v_exp_f32_e32 v241, v104
	v_exp_f32_e32 v243, v105
	v_mfma_f32_32x32x16_bf16 v[50:65], v[114:117], v[202:205], v[50:65]
	v_cvt_pk_bf16_f32 v193, v241, v243
	v_add_f32_e32 v213, v241, v213
	v_add_f32_e32 v213, v243, v213
	v_mfma_f32_32x32x16_bf16 v[2:17], v[122:125], v[202:205], v[2:17]
	v_exp_f32_e32 v245, v106
	v_exp_f32_e32 v247, v107
	s_waitcnt lgkmcnt(0)
	v_mfma_f32_32x32x16_bf16 v[18:33], v[118:121], v[194:197], v[18:33]
	ds_read_b128 v[98:101], v210 offset:512
	v_cvt_pk_bf16_f32 v186, v245, v247
	v_add_f32_e32 v213, v245, v213
	v_add_f32_e32 v213, v247, v213
	v_exp_f32_e32 v249, v108
	v_exp_f32_e32 v217, v109
	v_mfma_f32_32x32x16_bf16 v[34:49], v[126:129], v[194:197], v[34:49]
	v_cvt_pk_bf16_f32 v187, v249, v217
	v_add_f32_e32 v213, v249, v213
	v_add_f32_e32 v213, v217, v213
	v_exp_f32_e32 v219, v110
	v_exp_f32_e32 v221, v111
	v_mfma_f32_32x32x16_bf16 v[50:65], v[118:121], v[206:209], v[50:65]
	ds_read_b128 v[194:197], v210 offset:2560
	v_cvt_pk_bf16_f32 v188, v219, v221
	v_add_f32_e32 v213, v219, v213
	v_add_f32_e32 v213, v221, v213
	v_exp_f32_e32 v223, v112
	v_exp_f32_e32 v225, v113
	v_mfma_f32_32x32x16_bf16 v[2:17], v[126:129], v[206:209], v[2:17]
	v_cvt_pk_bf16_f32 v189, v223, v225
	v_add_f32_e32 v213, v223, v213
	v_add_f32_e32 v213, v225, v213
	s_add_i32 s33, s13, 1
	s_waitcnt vmcnt(0)
	s_and_b32 s34, s33, 3
	s_add_i32 s31, s31, 1
	s_cmpk_eq_i32 s31, 0x104
	s_waitcnt vmcnt(0) lgkmcnt(0)
	s_barrier
	s_cbranch_scc1 .LBB0_931
	s_mov_b32 s33, s30
	s_mov_b32 s30, s12
	s_mov_b32 s12, s13
	s_mov_b32 s13, s34
	s_branch .LBB0_927
.LBB0_931:
	v_mov_b32_e32 v202, v212
	v_mov_b32_e32 v203, v213
	ds_read_b128 v[66:69], v235 offset:16384
	ds_read_b128 v[70:73], v235 offset:16896
	v_mov_b32_e32 v0, v230
	s_movk_i32 s54, 0x6000
	v_mov_b32_e32 v224, 0x358637bd
	s_waitcnt lgkmcnt(1)
	v_mfma_f32_32x32x16_bf16 v[18:33], v[66:69], v[178:181], v[18:33]
	s_waitcnt lgkmcnt(0)
	v_mfma_f32_32x32x16_bf16 v[34:49], v[70:73], v[178:181], v[34:49]
	v_mfma_f32_32x32x16_bf16 v[50:65], v[66:69], v[190:193], v[50:65]
	v_mfma_f32_32x32x16_bf16 v[2:17], v[70:73], v[190:193], v[2:17]
	ds_read_b128 v[66:69], v235 offset:18432
	ds_read_b128 v[70:73], v235 offset:18944
	s_nop 0
	v_readfirstlane_b32 s10, v0
	s_andn2_b32 s10, s10, 63
	s_cmpk_lt_i32 s10, 0x200
	s_waitcnt lgkmcnt(1)
	v_mfma_f32_32x32x16_bf16 v[18:33], v[66:69], v[182:185], v[18:33]
	s_waitcnt lgkmcnt(0)
	v_mfma_f32_32x32x16_bf16 v[34:49], v[70:73], v[182:185], v[34:49]
	v_mfma_f32_32x32x16_bf16 v[50:65], v[66:69], v[186:189], v[50:65]
	v_mbcnt_lo_u32_b32 v66, -1, 0
	v_mbcnt_hi_u32_b32 v66, -1, v66
	v_mbcnt_lo_u32_b32 v67, -1, 0
	v_mbcnt_hi_u32_b32 v67, -1, v67
	s_nop 0
	v_lshlrev_b32_e32 v66, 2, v66
	v_lshlrev_b32_e32 v67, 2, v67
	v_xor_b32_e32 v66, 0x80, v66
	v_xor_b32_e32 v67, 0x80, v67
	v_mfma_f32_32x32x16_bf16 v[2:17], v[70:73], v[186:189], v[2:17]
	ds_bpermute_b32 v66, v66, v202
	ds_bpermute_b32 v67, v67, v203
	s_cbranch_scc0 .LBB0_919
	s_lshl_b64 s[6:7], s[6:7], 11
	s_waitcnt lgkmcnt(1)
	v_add_f32_e32 v66, v202, v66
	s_add_u32 s6, s2, s6
	v_rcp_f32_e32 v66, v66
	s_addc_u32 s7, s3, s7
	s_lshl_b32 s11, s21, 7
	v_and_or_b32 v68, v0, 31, s10
	s_add_u32 s6, s6, s11
	v_ashrrev_i32_e32 v69, 31, v68
	s_addc_u32 s7, s7, 0
	s_waitcnt lgkmcnt(0)
	v_add_f32_e32 v67, v203, v67
	v_lshlrev_b64 v[68:69], 11, v[68:69]
	v_lshrrev_b32_e32 v0, 2, v0
	v_lshl_add_u64 v[68:69], s[6:7], 0, v[68:69]
	v_pk_mul_f32 v[18:19], v[18:19], v[66:67] op_sel_hi:[1,0]
	v_pk_mul_f32 v[20:21], v[20:21], v[66:67] op_sel_hi:[1,0]
	v_and_b32_e32 v0, 8, v0
	v_rcp_f32_e32 v70, v67
	v_pk_mul_f32 v[34:35], v[34:35], v[66:67] op_sel_hi:[1,0]
	v_pk_mul_f32 v[36:37], v[36:37], v[66:67] op_sel_hi:[1,0]
	v_pk_mul_f32 v[38:39], v[38:39], v[66:67] op_sel_hi:[1,0]
	v_pk_mul_f32 v[40:41], v[40:41], v[66:67] op_sel_hi:[1,0]
	v_pk_mul_f32 v[42:43], v[42:43], v[66:67] op_sel_hi:[1,0]
	v_pk_mul_f32 v[44:45], v[44:45], v[66:67] op_sel_hi:[1,0]
	v_pk_mul_f32 v[46:47], v[46:47], v[66:67] op_sel_hi:[1,0]
	v_pk_mul_f32 v[48:49], v[48:49], v[66:67] op_sel_hi:[1,0]
	v_pk_mul_f32 v[22:23], v[22:23], v[66:67] op_sel_hi:[1,0]
	v_pk_mul_f32 v[24:25], v[24:25], v[66:67] op_sel_hi:[1,0]
	v_pk_mul_f32 v[26:27], v[26:27], v[66:67] op_sel_hi:[1,0]
	v_pk_mul_f32 v[28:29], v[28:29], v[66:67] op_sel_hi:[1,0]
	v_pk_mul_f32 v[30:31], v[30:31], v[66:67] op_sel_hi:[1,0]
	v_pk_mul_f32 v[32:33], v[32:33], v[66:67] op_sel_hi:[1,0]
	v_lshl_add_u64 v[66:67], v[68:69], 0, v[0:1]
	v_cvt_pk_bf16_f32 v18, v18, v19
	v_cvt_pk_bf16_f32 v19, v20, v21
	v_cvt_pk_bf16_f32 v20, v34, v35
	v_cvt_pk_bf16_f32 v21, v36, v37
	global_store_dwordx2 v[66:67], v[18:19], off offset:512
	global_store_dwordx2 v[66:67], v[20:21], off offset:576
	v_cvt_pk_bf16_f32 v18, v22, v23
	v_cvt_pk_bf16_f32 v19, v24, v25
	v_cvt_pk_bf16_f32 v20, v38, v39
	v_cvt_pk_bf16_f32 v21, v40, v41
	global_store_dwordx2 v[66:67], v[18:19], off offset:528
	global_store_dwordx2 v[66:67], v[20:21], off offset:592
	v_cvt_pk_bf16_f32 v18, v26, v27
	v_cvt_pk_bf16_f32 v19, v28, v29
	v_cvt_pk_bf16_f32 v20, v42, v43
	v_cvt_pk_bf16_f32 v21, v44, v45
	global_store_dwordx2 v[66:67], v[18:19], off offset:544
	global_store_dwordx2 v[66:67], v[20:21], off offset:608
	v_cvt_pk_bf16_f32 v18, v30, v31
	v_cvt_pk_bf16_f32 v19, v32, v33
	s_mov_b64 s[6:7], 0x10200
	v_cvt_pk_bf16_f32 v20, v46, v47
	v_cvt_pk_bf16_f32 v21, v48, v49
	global_store_dwordx2 v[66:67], v[18:19], off offset:560
	global_store_dwordx2 v[66:67], v[20:21], off offset:624
	v_lshl_add_u64 v[18:19], v[66:67], 0, s[6:7]
	s_mov_b64 s[6:7], 0x10240
	v_pk_mul_f32 v[2:3], v[2:3], v[70:71] op_sel_hi:[1,0]
	v_pk_mul_f32 v[4:5], v[4:5], v[70:71] op_sel_hi:[1,0]
	v_lshl_add_u64 v[20:21], v[66:67], 0, s[6:7]
	s_mov_b32 s6, 0x10000
	v_pk_mul_f32 v[50:51], v[50:51], v[70:71] op_sel_hi:[1,0]
	v_pk_mul_f32 v[52:53], v[52:53], v[70:71] op_sel_hi:[1,0]
	v_cvt_pk_bf16_f32 v2, v2, v3
	v_cvt_pk_bf16_f32 v3, v4, v5
	v_add_co_u32_e32 v4, vcc, s6, v66
	v_pk_mul_f32 v[54:55], v[54:55], v[70:71] op_sel_hi:[1,0]
	v_pk_mul_f32 v[56:57], v[56:57], v[70:71] op_sel_hi:[1,0]
	v_cvt_pk_bf16_f32 v22, v50, v51
	v_cvt_pk_bf16_f32 v23, v52, v53
	v_addc_co_u32_e32 v5, vcc, 0, v67, vcc
	v_pk_mul_f32 v[6:7], v[6:7], v[70:71] op_sel_hi:[1,0]
	v_pk_mul_f32 v[8:9], v[8:9], v[70:71] op_sel_hi:[1,0]
	v_pk_mul_f32 v[58:59], v[58:59], v[70:71] op_sel_hi:[1,0]
	v_pk_mul_f32 v[60:61], v[60:61], v[70:71] op_sel_hi:[1,0]
	global_store_dwordx2 v[4:5], v[22:23], off offset:512
	global_store_dwordx2 v[4:5], v[2:3], off offset:576
	v_cvt_pk_bf16_f32 v2, v54, v55
	v_cvt_pk_bf16_f32 v3, v56, v57
	v_pk_mul_f32 v[10:11], v[10:11], v[70:71] op_sel_hi:[1,0]
	v_pk_mul_f32 v[12:13], v[12:13], v[70:71] op_sel_hi:[1,0]
	v_pk_mul_f32 v[62:63], v[62:63], v[70:71] op_sel_hi:[1,0]
	v_pk_mul_f32 v[64:65], v[64:65], v[70:71] op_sel_hi:[1,0]
	v_cvt_pk_bf16_f32 v4, v6, v7
	v_cvt_pk_bf16_f32 v5, v8, v9
	global_store_dwordx2 v[18:19], v[2:3], off offset:16
	global_store_dwordx2 v[20:21], v[4:5], off offset:16
	v_cvt_pk_bf16_f32 v2, v58, v59
	v_cvt_pk_bf16_f32 v3, v60, v61
	v_pk_mul_f32 v[14:15], v[14:15], v[70:71] op_sel_hi:[1,0]
	v_pk_mul_f32 v[16:17], v[16:17], v[70:71] op_sel_hi:[1,0]
	v_cvt_pk_bf16_f32 v4, v10, v11
	v_cvt_pk_bf16_f32 v5, v12, v13
	global_store_dwordx2 v[18:19], v[2:3], off offset:32
	global_store_dwordx2 v[20:21], v[4:5], off offset:32
	v_cvt_pk_bf16_f32 v2, v62, v63
	v_cvt_pk_bf16_f32 v3, v64, v65
	v_cvt_pk_bf16_f32 v4, v14, v15
	v_cvt_pk_bf16_f32 v5, v16, v17
	global_store_dwordx2 v[18:19], v[2:3], off offset:48
	global_store_dwordx2 v[20:21], v[4:5], off offset:48
	s_branch .LBB0_919

.LBB0_952:
	s_lshr_b32 s11, s19, 3
	s_and_b32 s10, s19, 31
	s_and_b32 s11, s11, 0xffffe0
	s_or_b32 s10, s11, s10
	s_bfe_u32 s25, s19, 0x10007
	s_lshl_b32 s10, s10, 8
	s_bfe_u32 s26, s19, 0x20005
	s_lshl_b32 s11, s25, 14
	s_ashr_i32 s20, s10, 31
	s_add_u32 s10, s10, s11
	s_addc_u32 s11, s20, 0
	s_lshl_b64 s[20:21], s[10:11], 9
	s_add_u32 s22, s12, s20
	s_addc_u32 s21, s13, s21
	s_lshl_b32 s20, s26, 6
	s_lshl_b32 s23, s26, 7
	s_add_u32 s22, s22, s23
	s_addc_u32 s23, s21, 0
	s_lshl_b32 s21, s25, 2
	s_or_b32 s21, s21, s26
	s_mul_i32 s21, s21, 0x208000
	s_add_u32 s25, s14, s21
	s_addc_u32 s26, s15, 0
	v_mov_b32_e32 v4, v230
	s_add_u32 s27, s16, s21
	s_addc_u32 s28, s17, 0
	v_readfirstlane_b32 s21, v4
	v_and_b32_e32 v18, 31, v4
	s_ashr_i32 s21, s21, 6
	s_cmp_lt_i32 s21, 8
	v_lshl_or_b32 v0, s21, 5, v18
	v_ashrrev_i32_e32 v2, 31, v0
	s_cselect_b64 vcc, -1, 0
	v_cndmask_b32_e32 v3, 0, v2, vcc
	v_cndmask_b32_e32 v2, v18, v0, vcc
	v_bfe_u32 v5, v4, 5, 1
	v_lshlrev_b64 v[2:3], 9, v[2:3]
	v_lshl_add_u64 v[2:3], s[22:23], 0, v[2:3]
	v_lshlrev_b32_e32 v0, 4, v5
	v_lshl_add_u64 v[2:3], v[2:3], 0, v[0:1]
	global_load_dwordx4 v[130:133], v[2:3], off
	global_load_dwordx4 v[134:137], v[2:3], off offset:64
	global_load_dwordx4 v[138:141], v[2:3], off offset:32
	global_load_dwordx4 v[142:145], v[2:3], off offset:96
	s_lshl_b32 s29, s21, 10
	s_ashr_i32 s30, s29, 31
	v_and_b32_e32 v0, 63, v4
	v_and_b32_e32 v2, 19, v4
	v_lshlrev_b32_e32 v3, 1, v4
	v_lshrrev_b32_e32 v4, 1, v4
	s_add_u32 s22, s25, s29
	v_and_b32_e32 v3, 8, v3
	v_and_b32_e32 v4, 4, v4
	s_addc_u32 s23, s26, s30
	s_add_i32 s21, s29, 0
	v_lshlrev_b32_e32 v19, 10, v5
	v_or3_b32 v2, v2, v3, v4
	v_lshlrev_b32_e32 v0, 4, v0
	s_add_u32 s26, s27, s29
	s_mov_b32 m0, s21
	v_lshl_or_b32 v2, v2, 4, v19
	v_lshl_add_u64 v[174:175], s[22:23], 0, v[0:1]
	global_load_lds_dwordx4 v0, s[22:23]
	s_addc_u32 s27, s28, s30
	s_add_i32 m0, s21, 0x2000
	s_mov_b64 s[22:23], 0x2000
	v_add_u32_e32 v188, 0, v2
	v_lshl_add_u64 v[176:177], s[26:27], 0, v[0:1]
	global_load_lds_dwordx4 v0, s[26:27]
	v_lshl_add_u64 v[2:3], v[174:175], 0, s[22:23]
	s_add_i32 m0, s21, 0x4000
	v_mov_b32_e32 v150, v1
	global_load_lds_dwordx4 v[2:3], off
	v_lshl_add_u64 v[2:3], v[176:177], 0, s[22:23]
	s_add_i32 m0, s21, 0x6000
	v_lshl_or_b32 v0, v18, 4, v19
	global_load_lds_dwordx4 v[2:3], off
	s_waitcnt vmcnt(0)
	s_waitcnt vmcnt(0) lgkmcnt(0)
	s_barrier
	ds_read_b128 v[2:5], v188
	ds_read_b128 v[6:9], v188 offset:4096
	ds_read_b128 v[98:101], v188 offset:512
	ds_read_b128 v[10:13], v188 offset:2048
	ds_read_b128 v[102:105], v188 offset:4608
	ds_read_b128 v[14:17], v188 offset:6144
	ds_read_b128 v[162:165], v188 offset:2560
	ds_read_b128 v[166:169], v188 offset:6656
	s_mov_b32 s22, 2
	s_mov_b32 s23, 1
	s_mov_b32 s27, 0
	s_mov_b32 s25, 0
	s_mov_b32 s26, 0
	v_add_u32_e32 v0, 0, v0
	v_mov_b32_e32 v151, v150
	v_mov_b32_e32 v152, v150
	v_mov_b32_e32 v153, v150
	v_mov_b32_e32 v154, v150
	v_mov_b32_e32 v155, v150
	v_mov_b32_e32 v156, v150
	v_mov_b32_e32 v157, v150
	s_waitcnt lgkmcnt(7)
	v_mfma_f32_32x32x16_bf16 v[82:97], v[2:5], v[130:133], 0
	v_mov_b32_e32 v2, 0
	v_mov_b32_e32 v3, v2
	v_mov_b32_e32 v4, v2
	v_mov_b32_e32 v5, v2
	v_mov_b32_e32 v18, v2
	v_mov_b32_e32 v19, v2
	v_mov_b32_e32 v20, v2
	s_waitcnt lgkmcnt(6)
	v_mfma_f32_32x32x16_bf16 v[66:81], v[6:9], v[134:137], 0
	v_mov_b32_e32 v6, v2
	v_mov_b32_e32 v7, v2
	v_mov_b32_e32 v8, v2
	v_mov_b32_e32 v9, v2
	v_mov_b32_e32 v21, v2
	v_mov_b32_e32 v22, v2
	v_mov_b32_e32 v23, v2
	s_waitcnt lgkmcnt(4)
	v_mfma_f32_32x32x16_bf16 v[82:97], v[10:13], v[138:141], v[82:97]
	v_mov_b32_e32 v10, v2
	v_mov_b32_e32 v11, v2
	v_mov_b32_e32 v12, v2
	v_mov_b32_e32 v13, v2
	v_mov_b32_e32 v24, v2
	v_mov_b32_e32 v25, v2
	v_mov_b32_e32 v26, v2
	s_waitcnt lgkmcnt(2)
	v_mfma_f32_32x32x16_bf16 v[66:81], v[14:17], v[142:145], v[66:81]
	v_mov_b32_e32 v14, v2
	v_mov_b32_e32 v15, v2
	v_mov_b32_e32 v16, v2
	v_mov_b32_e32 v17, v2
	v_mov_b32_e32 v27, v2
	v_mov_b32_e32 v28, v2
	v_mov_b32_e32 v29, v2
	v_mov_b32_e32 v30, v2
	v_mov_b32_e32 v31, v2
	v_mov_b32_e32 v32, v2
	v_mov_b32_e32 v33, v2
	v_mov_b32_e32 v158, v150
	v_mov_b32_e32 v159, v150
	v_mov_b32_e32 v160, v150
	v_mov_b32_e32 v161, v150
	v_mov_b32_e32 v146, v150
	v_mov_b32_e32 v147, v150
	v_mov_b32_e32 v148, v150
	v_mov_b32_e32 v149, v150
	v_mov_b32_e32 v34, v2
	v_mov_b32_e32 v35, v2
	v_mov_b32_e32 v36, v2
	v_mov_b32_e32 v37, v2
	v_mov_b32_e32 v38, v2
	v_mov_b32_e32 v39, v2
	v_mov_b32_e32 v40, v2
	v_mov_b32_e32 v41, v2
	v_mov_b32_e32 v42, v2
	v_mov_b32_e32 v43, v2
	v_mov_b32_e32 v44, v2
	v_mov_b32_e32 v45, v2
	v_mov_b32_e32 v46, v2
	v_mov_b32_e32 v47, v2
	v_mov_b32_e32 v48, v2
	v_mov_b32_e32 v49, v2
	v_mov_b32_e32 v50, v2
	v_mov_b32_e32 v51, v2
	v_mov_b32_e32 v52, v2
	v_mov_b32_e32 v53, v2
	v_mov_b32_e32 v54, v2
	v_mov_b32_e32 v55, v2
	v_mov_b32_e32 v56, v2
	v_mov_b32_e32 v57, v2
	v_mov_b32_e32 v58, v2
	v_mov_b32_e32 v59, v2
	v_mov_b32_e32 v60, v2
	v_mov_b32_e32 v61, v2
	v_mov_b32_e32 v62, v2
	v_mov_b32_e32 v63, v2
	v_mov_b32_e32 v64, v2
	v_mov_b32_e32 v65, v2
	v_mov_b32_e32 v178, v2
	v_mov_b32_e32 v179, v2
	v_mov_b32_e32 v232, v178
	v_mov_b32_e32 v233, v179
.LBB0_953:
	s_min_i32 s28, s26, 0x101
	s_lshl_b32 s28, s28, 13
	s_add_i32 s88, s28, 0x4000
	s_lshl_b32 s28, s22, 14
	s_add_i32 s28, s21, s28
	v_lshl_add_u64 v[106:107], v[174:175], 0, s[88:89]
	s_mov_b32 m0, s28
	v_lshl_add_u32 v181, s27, 14, v0
	global_load_lds_dwordx4 v[106:107], off
	v_lshl_add_u64 v[106:107], v[176:177], 0, s[88:89]
	s_add_i32 m0, s28, 0x2000
	s_lshl_b32 s28, s25, 14
	global_load_lds_dwordx4 v[106:107], off
	ds_read_b128 v[190:193], v181 offset:12288
	v_add_u32_e32 v189, s28, v0
	v_lshl_add_u32 v210, s23, 14, v188
	v_mfma_f32_32x32x16_bf16 v[114:129], v[98:101], v[130:133], 0
	v_exp_f32_e32 v194, v82
	v_exp_f32_e32 v196, v83
	v_exp_f32_e32 v198, v84
	v_exp_f32_e32 v200, v85
	v_mfma_f32_32x32x16_bf16 v[98:113], v[102:105], v[134:137], 0
	ds_read_b128 v[82:85], v181 offset:12800
	v_cvt_pk_bf16_f32 v170, v194, v196
	v_add_f32_e32 v232, v194, v232
	v_add_f32_e32 v232, v196, v232
	v_cvt_pk_bf16_f32 v171, v198, v200
	v_add_f32_e32 v232, v198, v232
	v_add_f32_e32 v232, v200, v232
	v_exp_f32_e32 v202, v86
	v_exp_f32_e32 v204, v87
	s_waitcnt lgkmcnt(0)
	v_mfma_f32_32x32x16_bf16 v[114:129], v[162:165], v[138:141], v[114:129]
	v_cvt_pk_bf16_f32 v172, v202, v204
	v_add_f32_e32 v232, v202, v232
	v_add_f32_e32 v232, v204, v232
	v_exp_f32_e32 v206, v88
	v_exp_f32_e32 v208, v89
	v_mfma_f32_32x32x16_bf16 v[98:113], v[166:169], v[142:145], v[98:113]
	v_exp_f32_e32 v168, v92
	v_exp_f32_e32 v166, v93
	v_cvt_pk_bf16_f32 v173, v206, v208
	v_add_f32_e32 v232, v206, v232
	v_add_f32_e32 v232, v208, v232
	v_exp_f32_e32 v214, v90
	v_exp_f32_e32 v216, v91
	v_mfma_f32_32x32x16_bf16 v[34:49], v[190:193], v[150:153], v[34:49]
	ds_read_b128 v[86:89], v181 offset:14336
	v_cvt_pk_bf16_f32 v162, v214, v216
	v_add_f32_e32 v232, v214, v232
	v_add_f32_e32 v232, v216, v232
	v_cvt_pk_bf16_f32 v163, v168, v166
	v_add_f32_e32 v232, v168, v232
	v_add_f32_e32 v232, v166, v232
	v_exp_f32_e32 v182, v94
	v_exp_f32_e32 v180, v95
	v_mfma_f32_32x32x16_bf16 v[50:65], v[82:85], v[150:153], v[50:65]
	ds_read_b128 v[90:93], v181 offset:14848
	v_cvt_pk_bf16_f32 v164, v182, v180
	v_add_f32_e32 v232, v182, v232
	v_add_f32_e32 v232, v180, v232
	v_exp_f32_e32 v186, v96
	v_exp_f32_e32 v184, v97
	v_mfma_f32_32x32x16_bf16 v[2:17], v[190:193], v[158:161], v[2:17]
	v_cvt_pk_bf16_f32 v165, v186, v184
	v_add_f32_e32 v232, v186, v232
	v_add_f32_e32 v232, v184, v232
	v_exp_f32_e32 v195, v66
	v_exp_f32_e32 v197, v67
	v_exp_f32_e32 v199, v68
	v_exp_f32_e32 v201, v69
	v_mfma_f32_32x32x16_bf16 v[18:33], v[82:85], v[158:161], v[18:33]
	v_cvt_pk_bf16_f32 v158, v195, v197
	v_add_f32_e32 v233, v195, v233
	v_add_f32_e32 v233, v197, v233
	v_cvt_pk_bf16_f32 v159, v199, v201
	v_add_f32_e32 v233, v199, v233
	v_add_f32_e32 v233, v201, v233
	v_exp_f32_e32 v203, v70
	v_exp_f32_e32 v205, v71
	s_waitcnt lgkmcnt(0)
	v_mfma_f32_32x32x16_bf16 v[34:49], v[86:89], v[154:157], v[34:49]
	ds_read_b128 v[66:69], v210
	v_cvt_pk_bf16_f32 v160, v203, v205
	v_add_f32_e32 v233, v203, v233
	v_add_f32_e32 v233, v205, v233
	v_exp_f32_e32 v207, v72
	v_exp_f32_e32 v209, v73
	v_mfma_f32_32x32x16_bf16 v[50:65], v[90:93], v[154:157], v[50:65]
	ds_read_b128 v[70:73], v210 offset:4096
	v_exp_f32_e32 v169, v76
	v_exp_f32_e32 v167, v77
	v_cvt_pk_bf16_f32 v161, v207, v209
	v_add_f32_e32 v233, v207, v233
	v_add_f32_e32 v233, v209, v233
	v_exp_f32_e32 v215, v74
	v_exp_f32_e32 v217, v75
	v_mfma_f32_32x32x16_bf16 v[2:17], v[86:89], v[146:149], v[2:17]
	ds_read_b128 v[152:155], v210 offset:2048
	v_cvt_pk_bf16_f32 v190, v215, v217
	v_add_f32_e32 v233, v215, v233
	v_add_f32_e32 v233, v217, v233
	v_cvt_pk_bf16_f32 v191, v169, v167
	v_add_f32_e32 v233, v169, v233
	v_add_f32_e32 v233, v167, v233
	v_exp_f32_e32 v183, v78
	v_exp_f32_e32 v181, v79
	v_mfma_f32_32x32x16_bf16 v[18:33], v[90:93], v[146:149], v[18:33]
	v_exp_f32_e32 v187, v80
	v_exp_f32_e32 v185, v81
	ds_read_b128 v[194:197], v210 offset:6144
	v_cvt_pk_bf16_f32 v192, v183, v181
	v_add_f32_e32 v233, v183, v233
	v_add_f32_e32 v233, v181, v233
	v_cvt_pk_bf16_f32 v193, v187, v185
	v_add_f32_e32 v233, v187, v233
	v_add_f32_e32 v233, v185, v233
	s_waitcnt lgkmcnt(0)
	v_mfma_f32_32x32x16_bf16 v[82:97], v[66:69], v[130:133], 0
	ds_read_b128 v[146:149], v189 offset:8192
	v_exp_f32_e32 v198, v114
	v_exp_f32_e32 v200, v115
	v_exp_f32_e32 v202, v116
	v_exp_f32_e32 v204, v117
	v_mfma_f32_32x32x16_bf16 v[66:81], v[70:73], v[134:137], 0
	ds_read_b128 v[114:117], v189 offset:8704
	v_cvt_pk_bf16_f32 v150, v198, v200
	v_add_f32_e32 v232, v198, v232
	v_add_f32_e32 v232, v200, v232
	v_cvt_pk_bf16_f32 v151, v202, v204
	v_add_f32_e32 v232, v202, v232
	v_add_f32_e32 v232, v204, v232
	v_exp_f32_e32 v206, v118
	v_exp_f32_e32 v208, v119
	v_mfma_f32_32x32x16_bf16 v[82:97], v[152:155], v[138:141], v[82:97]
	v_cvt_pk_bf16_f32 v152, v206, v208
	v_add_f32_e32 v232, v206, v232
	v_add_f32_e32 v232, v208, v232
	v_exp_f32_e32 v214, v120
	v_exp_f32_e32 v216, v121
	v_mfma_f32_32x32x16_bf16 v[66:81], v[194:197], v[142:145], v[66:81]
	v_cvt_pk_bf16_f32 v153, v214, v216
	v_add_f32_e32 v232, v214, v232
	v_add_f32_e32 v232, v216, v232
	v_exp_f32_e32 v194, v122
	v_exp_f32_e32 v196, v123
	v_exp_f32_e32 v218, v124
	v_exp_f32_e32 v220, v125
	s_waitcnt lgkmcnt(0)
	v_mfma_f32_32x32x16_bf16 v[34:49], v[146:149], v[170:173], v[34:49]
	ds_read_b128 v[118:121], v189 offset:10240
	v_cvt_pk_bf16_f32 v154, v194, v196
	v_add_f32_e32 v232, v194, v232
	v_add_f32_e32 v232, v196, v232
	v_cvt_pk_bf16_f32 v155, v218, v220
	v_add_f32_e32 v232, v218, v232
	v_add_f32_e32 v232, v220, v232
	v_exp_f32_e32 v126, v126
	v_exp_f32_e32 v222, v127
	v_mfma_f32_32x32x16_bf16 v[50:65], v[114:117], v[170:173], v[50:65]
	ds_read_b128 v[122:125], v189 offset:10752
	v_cvt_pk_bf16_f32 v156, v126, v222
	v_add_f32_e32 v232, v126, v232
	v_add_f32_e32 v232, v222, v232
	v_exp_f32_e32 v128, v128
	v_exp_f32_e32 v170, v129
	v_mfma_f32_32x32x16_bf16 v[2:17], v[146:149], v[158:161], v[2:17]
	v_cvt_pk_bf16_f32 v157, v128, v170
	v_add_f32_e32 v232, v128, v232
	v_add_f32_e32 v232, v170, v232
	v_exp_f32_e32 v199, v98
	v_exp_f32_e32 v201, v99
	v_exp_f32_e32 v203, v100
	v_exp_f32_e32 v205, v101
	v_mfma_f32_32x32x16_bf16 v[18:33], v[114:117], v[158:161], v[18:33]
	v_cvt_pk_bf16_f32 v158, v199, v201
	v_add_f32_e32 v233, v199, v233
	v_add_f32_e32 v233, v201, v233
	v_cvt_pk_bf16_f32 v159, v203, v205
	v_add_f32_e32 v233, v203, v233
	v_add_f32_e32 v233, v205, v233
	v_exp_f32_e32 v207, v102
	v_exp_f32_e32 v209, v103
	s_waitcnt lgkmcnt(0)
	v_mfma_f32_32x32x16_bf16 v[34:49], v[118:121], v[162:165], v[34:49]
	ds_read_b128 v[98:101], v210 offset:512
	v_cvt_pk_bf16_f32 v160, v207, v209
	v_add_f32_e32 v233, v207, v233
	v_add_f32_e32 v233, v209, v233
	v_exp_f32_e32 v215, v104
	v_exp_f32_e32 v217, v105
	v_mfma_f32_32x32x16_bf16 v[50:65], v[122:125], v[162:165], v[50:65]
	ds_read_b128 v[102:105], v210 offset:4608
	v_cvt_pk_bf16_f32 v161, v215, v217
	v_add_f32_e32 v233, v215, v233
	v_add_f32_e32 v233, v217, v233
	v_exp_f32_e32 v195, v106
	v_exp_f32_e32 v197, v107
	v_exp_f32_e32 v219, v108
	v_exp_f32_e32 v221, v109
	v_mfma_f32_32x32x16_bf16 v[2:17], v[118:121], v[190:193], v[2:17]
	ds_read_b128 v[162:165], v210 offset:2560
	v_cvt_pk_bf16_f32 v146, v195, v197
	v_add_f32_e32 v233, v195, v233
	v_add_f32_e32 v233, v197, v233
	v_cvt_pk_bf16_f32 v147, v219, v221
	v_add_f32_e32 v233, v219, v233
	v_add_f32_e32 v233, v221, v233
	v_exp_f32_e32 v127, v110
	v_exp_f32_e32 v223, v111
	v_mfma_f32_32x32x16_bf16 v[18:33], v[122:125], v[190:193], v[18:33]
	v_exp_f32_e32 v129, v112
	ds_read_b128 v[166:169], v210 offset:6656
	v_exp_f32_e32 v171, v113
	v_cvt_pk_bf16_f32 v148, v127, v223
	v_add_f32_e32 v233, v127, v233
	v_add_f32_e32 v233, v223, v233
	v_cvt_pk_bf16_f32 v149, v129, v171
	v_add_f32_e32 v233, v129, v233
	v_add_f32_e32 v233, v171, v233
	s_add_i32 s27, s22, 1
	s_waitcnt vmcnt(0)
	s_and_b32 s28, s27, 3
	s_add_i32 s26, s26, 1
	s_cmpk_eq_i32 s26, 0x104
	s_mov_b32 s27, s25
	s_mov_b32 s25, s23
	s_mov_b32 s23, s22
	s_mov_b32 s22, s28
	s_waitcnt vmcnt(0) lgkmcnt(0)
	s_barrier
	s_cbranch_scc0 .LBB0_953
	v_mov_b32_e32 v178, v232
	v_mov_b32_e32 v179, v233
	ds_read_b128 v[66:69], v189 offset:12288
	ds_read_b128 v[70:73], v189 offset:12800
	v_mov_b32_e32 v0, v230
	s_waitcnt lgkmcnt(1)
	v_mfma_f32_32x32x16_bf16 v[34:49], v[66:69], v[150:153], v[34:49]
	s_waitcnt lgkmcnt(0)
	v_mfma_f32_32x32x16_bf16 v[50:65], v[70:73], v[150:153], v[50:65]
	v_mfma_f32_32x32x16_bf16 v[2:17], v[66:69], v[158:161], v[2:17]
	v_mfma_f32_32x32x16_bf16 v[18:33], v[70:73], v[158:161], v[18:33]
	ds_read_b128 v[68:71], v189 offset:14336
	ds_read_b128 v[72:75], v189 offset:14848
	v_mbcnt_lo_u32_b32 v76, -1, 0
	v_mbcnt_hi_u32_b32 v76, -1, v76
	v_mbcnt_lo_u32_b32 v77, -1, 0
	v_mbcnt_hi_u32_b32 v77, -1, v77
	global_load_dwordx2 v[66:67], v1, s[6:7]
	v_lshlrev_b32_e32 v77, 2, v77
	v_xor_b32_e32 v77, 0x80, v77
	v_lshlrev_b32_e32 v76, 2, v76
	ds_bpermute_b32 v77, v77, v179
	v_xor_b32_e32 v76, 0x80, v76
	ds_bpermute_b32 v76, v76, v178
	s_waitcnt lgkmcnt(3)
	v_mfma_f32_32x32x16_bf16 v[2:17], v[68:71], v[146:149], v[2:17]
	v_readfirstlane_b32 s21, v0
	s_ashr_i32 s21, s21, 1
	s_andn2_b32 s21, s21, 31
	s_cmpk_lt_i32 s21, 0x100
	s_waitcnt lgkmcnt(2)
	v_mfma_f32_32x32x16_bf16 v[18:33], v[72:75], v[146:149], v[18:33]
	v_mfma_f32_32x32x16_bf16 v[34:49], v[68:71], v[154:157], v[34:49]
	s_waitcnt lgkmcnt(1)
	v_add_f32_e32 v70, v179, v77
	v_mbcnt_lo_u32_b32 v68, -1, 0
	v_mbcnt_hi_u32_b32 v68, -1, v68
	v_rcp_f32_e32 v70, v70
	v_lshlrev_b32_e32 v69, 2, v68
	s_waitcnt lgkmcnt(0)
	v_add_f32_e32 v68, v178, v76
	v_rcp_f32_e32 v68, v68
	s_waitcnt vmcnt(0)
	v_mul_f32_e32 v66, v66, v70
	v_mfma_f32_32x32x16_bf16 v[50:65], v[72:75], v[154:157], v[50:65]
	v_mul_f32_e64 v2, v2, v66
	v_mul_f32_e64 v3, v3, v66
	v_mul_f32_e64 v18, v18, v66
	v_mul_f32_e64 v19, v19, v66
	v_mul_f32_e64 v4, v4, v66
	v_mul_f32_e64 v5, v5, v66
	v_pk_mul_f32 v[20:21], v[20:21], v[66:67] op_sel_hi:[1,0]
	v_pk_mul_f32 v[70:71], v[24:25], v[66:67] op_sel_hi:[1,0]
	v_pk_fma_f32 v[24:25], v[34:35], v[68:69], v[2:3] op_sel_hi:[1,0,1] neg_lo:[0,0,1] neg_hi:[0,0,1]
	v_pk_mul_f32 v[72:73], v[26:27], v[66:67] op_sel_hi:[1,0]
	s_nop 1
	v_pk_fma_f32 v[2:3], v[50:51], v[68:69], v[18:19] op_sel_hi:[1,0,1] neg_lo:[0,0,1] neg_hi:[0,0,1]
	v_pk_fma_f32 v[26:27], v[36:37], v[68:69], v[4:5] op_sel_hi:[1,0,1] neg_lo:[0,0,1] neg_hi:[0,0,1]
	v_pk_fma_f32 v[4:5], v[52:53], v[68:69], v[20:21] op_sel_hi:[1,0,1] neg_lo:[0,0,1] neg_hi:[0,0,1]
	v_pk_mul_f32 v[18:19], v[2:3], v[2:3]
	v_pk_mul_f32 v[6:7], v[6:7], v[66:67] op_sel_hi:[1,0]
	v_pk_mul_f32 v[22:23], v[22:23], v[66:67] op_sel_hi:[1,0]
	v_pk_mul_f32 v[36:37], v[4:5], v[4:5]
	v_pk_fma_f32 v[18:19], v[24:25], v[24:25], v[18:19]
	v_pk_mul_f32 v[74:75], v[28:29], v[66:67] op_sel_hi:[1,0]
	v_pk_fma_f32 v[28:29], v[38:39], v[68:69], v[6:7] op_sel_hi:[1,0,1] neg_lo:[0,0,1] neg_hi:[0,0,1]
	v_pk_fma_f32 v[6:7], v[54:55], v[68:69], v[22:23] op_sel_hi:[1,0,1] neg_lo:[0,0,1] neg_hi:[0,0,1]
	v_pk_fma_f32 v[36:37], v[26:27], v[26:27], v[36:37]
	v_add_f32_e32 v18, v18, v19
	v_pk_mul_f32 v[8:9], v[8:9], v[66:67] op_sel_hi:[1,0]
	v_pk_mul_f32 v[38:39], v[6:7], v[6:7]
	v_add_f32_e32 v18, v36, v18
	v_pk_mul_f32 v[76:77], v[30:31], v[66:67] op_sel_hi:[1,0]
	v_pk_fma_f32 v[30:31], v[40:41], v[68:69], v[8:9] op_sel_hi:[1,0,1] neg_lo:[0,0,1] neg_hi:[0,0,1]
	v_pk_fma_f32 v[8:9], v[56:57], v[68:69], v[70:71] op_sel_hi:[1,0,1] neg_lo:[0,0,1] neg_hi:[0,0,1]
	v_pk_fma_f32 v[38:39], v[28:29], v[28:29], v[38:39]
	v_add_f32_e32 v18, v37, v18
	v_pk_mul_f32 v[10:11], v[10:11], v[66:67] op_sel_hi:[1,0]
	v_pk_mul_f32 v[40:41], v[8:9], v[8:9]
	v_add_f32_e32 v18, v38, v18
	v_pk_mul_f32 v[78:79], v[32:33], v[66:67] op_sel_hi:[1,0]
	v_pk_fma_f32 v[32:33], v[42:43], v[68:69], v[10:11] op_sel_hi:[1,0,1] neg_lo:[0,0,1] neg_hi:[0,0,1]
	v_pk_fma_f32 v[10:11], v[58:59], v[68:69], v[72:73] op_sel_hi:[1,0,1] neg_lo:[0,0,1] neg_hi:[0,0,1]
	v_pk_fma_f32 v[40:41], v[30:31], v[30:31], v[40:41]
	v_add_f32_e32 v18, v39, v18
	v_pk_mul_f32 v[12:13], v[12:13], v[66:67] op_sel_hi:[1,0]
	v_pk_mul_f32 v[42:43], v[10:11], v[10:11]
	v_add_f32_e32 v18, v40, v18
	v_pk_fma_f32 v[34:35], v[44:45], v[68:69], v[12:13] op_sel_hi:[1,0,1] neg_lo:[0,0,1] neg_hi:[0,0,1]
	v_pk_fma_f32 v[12:13], v[60:61], v[68:69], v[74:75] op_sel_hi:[1,0,1] neg_lo:[0,0,1] neg_hi:[0,0,1]
	v_pk_fma_f32 v[42:43], v[32:33], v[32:33], v[42:43]
	v_add_f32_e32 v18, v41, v18
	v_pk_mul_f32 v[14:15], v[14:15], v[66:67] op_sel_hi:[1,0]
	v_pk_mul_f32 v[44:45], v[12:13], v[12:13]
	v_add_f32_e32 v18, v42, v18
	v_pk_fma_f32 v[20:21], v[46:47], v[68:69], v[14:15] op_sel_hi:[1,0,1] neg_lo:[0,0,1] neg_hi:[0,0,1]
	v_pk_fma_f32 v[14:15], v[62:63], v[68:69], v[76:77] op_sel_hi:[1,0,1] neg_lo:[0,0,1] neg_hi:[0,0,1]
	v_pk_fma_f32 v[44:45], v[34:35], v[34:35], v[44:45]
	v_add_f32_e32 v18, v43, v18
	v_pk_mul_f32 v[16:17], v[16:17], v[66:67] op_sel_hi:[1,0]
	v_pk_mul_f32 v[46:47], v[14:15], v[14:15]
	v_add_f32_e32 v18, v44, v18
	v_pk_fma_f32 v[22:23], v[48:49], v[68:69], v[16:17] op_sel_hi:[1,0,1] neg_lo:[0,0,1] neg_hi:[0,0,1]
	v_pk_fma_f32 v[16:17], v[64:65], v[68:69], v[78:79] op_sel_hi:[1,0,1] neg_lo:[0,0,1] neg_hi:[0,0,1]
	v_pk_fma_f32 v[46:47], v[20:21], v[20:21], v[46:47]
	v_add_f32_e32 v18, v45, v18
	v_pk_mul_f32 v[48:49], v[16:17], v[16:17]
	v_add_f32_e32 v18, v46, v18
	v_pk_fma_f32 v[48:49], v[22:23], v[22:23], v[48:49]
	v_add_f32_e32 v18, v47, v18
	v_add_f32_e32 v18, v48, v18
	v_add_f32_e32 v36, v49, v18
	v_xor_b32_e32 v18, 0x80, v69
	ds_bpermute_b32 v37, v18, v36
	s_cbranch_scc0 .LBB0_951
	s_waitcnt lgkmcnt(0)
	v_add_f32_e32 v36, v36, v37
	v_fmamk_f32 v36, v36, 0x3c800000, v224
	v_cmp_gt_f32_e32 vcc, s31, v36
	v_mul_f32_e32 v37, 0x4b800000, v36
	v_and_or_b32 v18, v0, 31, s21
	v_cndmask_b32_e32 v36, v36, v37, vcc
	v_rsq_f32_e32 v36, v36
	v_lshrrev_b32_e32 v0, 3, v0
	v_and_b32_e32 v0, 4, v0
	v_lshlrev_b32_e32 v41, 2, v0
	v_mul_f32_e32 v37, 0x45800000, v36
	v_cndmask_b32_e32 v36, v36, v37, vcc
	v_mul_f32_e32 v40, v67, v36
	global_load_dwordx4 v[36:39], v41, s[8:9] offset:128
	s_lshl_b64 s[10:11], s[10:11], 11
	s_add_u32 s10, s2, s10
	s_addc_u32 s11, s3, s11
	s_lshl_b32 s20, s20, 1
	s_add_u32 s10, s10, s20
	v_ashrrev_i32_e32 v19, 31, v18
	s_addc_u32 s11, s11, 0
	v_lshlrev_b64 v[18:19], 11, v[18:19]
	v_lshl_add_u64 v[18:19], s[10:11], 0, v[18:19]
	v_lshlrev_b32_e32 v0, 1, v0
	v_lshl_add_u64 v[18:19], v[18:19], 0, v[0:1]
	s_waitcnt vmcnt(0)
	v_pk_mul_f32 v[36:37], v[40:41], v[36:37] op_sel_hi:[0,1]
	v_pk_mul_f32 v[2:3], v[2:3], v[36:37]
	v_pk_mul_f32 v[36:37], v[40:41], v[38:39] op_sel_hi:[0,1]
	v_pk_mul_f32 v[4:5], v[4:5], v[36:37]
	global_load_dwordx4 v[36:39], v41, s[8:9] offset:160
	v_cvt_pk_bf16_f32 v2, v2, v3
	v_cvt_pk_bf16_f32 v3, v4, v5
	s_waitcnt vmcnt(0)
	v_pk_mul_f32 v[36:37], v[40:41], v[36:37] op_sel_hi:[0,1]
	v_pk_mul_f32 v[6:7], v[6:7], v[36:37]
	v_pk_mul_f32 v[36:37], v[40:41], v[38:39] op_sel_hi:[0,1]
	v_pk_mul_f32 v[8:9], v[8:9], v[36:37]
	global_load_dwordx4 v[36:39], v41, s[8:9] offset:192
	v_cvt_pk_bf16_f32 v4, v6, v7
	v_cvt_pk_bf16_f32 v5, v8, v9
	s_waitcnt vmcnt(0)
	v_pk_mul_f32 v[36:37], v[40:41], v[36:37] op_sel_hi:[0,1]
	v_pk_mul_f32 v[10:11], v[10:11], v[36:37]
	v_pk_mul_f32 v[36:37], v[40:41], v[38:39] op_sel_hi:[0,1]
	v_pk_mul_f32 v[12:13], v[12:13], v[36:37]
	global_load_dwordx4 v[36:39], v41, s[8:9] offset:224
	s_waitcnt vmcnt(0)
	v_pk_mul_f32 v[36:37], v[40:41], v[36:37] op_sel_hi:[0,1]
	v_pk_mul_f32 v[14:15], v[14:15], v[36:37]
	v_pk_mul_f32 v[36:37], v[40:41], v[38:39] op_sel_hi:[0,1]
	v_pk_mul_f32 v[16:17], v[16:17], v[36:37]
	global_load_dwordx4 v[36:39], v41, s[8:9]
	s_waitcnt vmcnt(0)
	v_pk_mul_f32 v[36:37], v[40:41], v[36:37] op_sel_hi:[0,1]
	v_pk_mul_f32 v[24:25], v[24:25], v[36:37]
	v_pk_mul_f32 v[36:37], v[40:41], v[38:39] op_sel_hi:[0,1]
	v_pk_mul_f32 v[26:27], v[26:27], v[36:37]
	global_load_dwordx4 v[36:39], v41, s[8:9] offset:32
	v_cvt_pk_bf16_f32 v24, v24, v25
	v_cvt_pk_bf16_f32 v25, v26, v27
	s_waitcnt vmcnt(0)
	v_pk_mul_f32 v[36:37], v[40:41], v[36:37] op_sel_hi:[0,1]
	v_pk_mul_f32 v[28:29], v[28:29], v[36:37]
	v_pk_mul_f32 v[36:37], v[40:41], v[38:39] op_sel_hi:[0,1]
	v_pk_mul_f32 v[30:31], v[30:31], v[36:37]
	global_load_dwordx4 v[36:39], v41, s[8:9] offset:64
	s_waitcnt vmcnt(0)
	v_pk_mul_f32 v[36:37], v[40:41], v[36:37] op_sel_hi:[0,1]
	v_pk_mul_f32 v[32:33], v[32:33], v[36:37]
	v_pk_mul_f32 v[36:37], v[40:41], v[38:39] op_sel_hi:[0,1]
	v_pk_mul_f32 v[34:35], v[34:35], v[36:37]
	global_load_dwordx4 v[36:39], v41, s[8:9] offset:96
	s_nop 0
	global_store_dwordx2 v[18:19], v[24:25], off offset:1024
	global_store_dwordx2 v[18:19], v[2:3], off offset:1088
	v_cvt_pk_bf16_f32 v2, v28, v29
	v_cvt_pk_bf16_f32 v3, v30, v31
	global_store_dwordx2 v[18:19], v[2:3], off offset:1040
	global_store_dwordx2 v[18:19], v[4:5], off offset:1104
	v_cvt_pk_bf16_f32 v2, v32, v33
	v_cvt_pk_bf16_f32 v3, v34, v35
	v_cvt_pk_bf16_f32 v4, v10, v11
	v_cvt_pk_bf16_f32 v5, v12, v13
	global_store_dwordx2 v[18:19], v[2:3], off offset:1056
	global_store_dwordx2 v[18:19], v[4:5], off offset:1120
	v_cvt_pk_bf16_f32 v4, v14, v15
	v_cvt_pk_bf16_f32 v5, v16, v17
	s_waitcnt vmcnt(6)
	v_pk_mul_f32 v[36:37], v[40:41], v[36:37] op_sel_hi:[0,1]
	v_pk_mul_f32 v[20:21], v[20:21], v[36:37]
	v_pk_mul_f32 v[36:37], v[40:41], v[38:39] op_sel_hi:[0,1]
	v_pk_mul_f32 v[22:23], v[22:23], v[36:37]
	v_cvt_pk_bf16_f32 v2, v20, v21
	v_cvt_pk_bf16_f32 v3, v22, v23
	global_store_dwordx2 v[18:19], v[2:3], off offset:1072
	global_store_dwordx2 v[18:19], v[4:5], off offset:1136
	s_branch .LBB0_951

.LBB0_966:
	s_ashr_i32 s16, s14, 7
	s_ashr_i32 s17, s16, 31
	s_lshl_b32 s15, s14, 8
	s_lshl_b64 s[6:7], s[16:17], 14
	s_and_b32 s15, s15, 0x3f00
	s_or_b32 s6, s6, s15
	s_bfe_u32 s19, s14, 0x10006
	s_lshl_b64 s[20:21], s[6:7], 9
	s_add_u32 s17, s8, s20
	s_addc_u32 s21, s9, s21
	s_lshl_b32 s15, s19, 7
	s_lshl_b32 s20, s19, 8
	s_add_u32 s20, s17, s20
	s_addc_u32 s21, s21, 0
	s_lshl_b32 s16, s16, 1
	s_or_b32 s16, s16, s19
	s_mul_hi_i32 s17, s16, 0x208000
	s_mul_i32 s16, s16, 0x208000
	s_add_u32 s19, s10, s16
	s_addc_u32 s22, s11, s17
	v_mov_b32_e32 v4, v230
	s_add_u32 s23, s12, s16
	s_addc_u32 s17, s13, s17
	v_readfirstlane_b32 s16, v4
	v_and_b32_e32 v14, 31, v4
	s_ashr_i32 s16, s16, 6
	s_cmp_lt_i32 s16, 8
	v_lshl_or_b32 v0, s16, 5, v14
	v_ashrrev_i32_e32 v2, 31, v0
	s_cselect_b64 vcc, -1, 0
	v_cndmask_b32_e32 v3, 0, v2, vcc
	v_cndmask_b32_e32 v2, v14, v0, vcc
	v_bfe_u32 v5, v4, 5, 1
	v_lshlrev_b64 v[2:3], 9, v[2:3]
	v_lshl_add_u64 v[2:3], s[20:21], 0, v[2:3]
	v_lshlrev_b32_e32 v0, 4, v5
	v_lshl_add_u64 v[2:3], v[2:3], 0, v[0:1]
	global_load_dwordx4 v[130:133], v[2:3], off
	global_load_dwordx4 v[134:137], v[2:3], off offset:128
	global_load_dwordx4 v[138:141], v[2:3], off offset:32
	global_load_dwordx4 v[142:145], v[2:3], off offset:160
	global_load_dwordx4 v[146:149], v[2:3], off offset:64
	global_load_dwordx4 v[150:153], v[2:3], off offset:192
	global_load_dwordx4 v[154:157], v[2:3], off offset:96
	global_load_dwordx4 v[158:161], v[2:3], off offset:224
	s_lshl_b32 s25, s16, 10
	s_ashr_i32 s26, s25, 31
	s_add_u32 s20, s19, s25
	v_and_b32_e32 v0, 63, v4
	s_addc_u32 s21, s22, s26
	s_add_i32 s16, s25, 0
	v_lshlrev_b32_e32 v0, 4, v0
	s_add_u32 s22, s23, s25
	s_mov_b32 m0, s16
	v_lshl_add_u64 v[194:195], s[20:21], 0, v[0:1]
	global_load_lds_dwordx4 v0, s[20:21]
	s_addc_u32 s23, s17, s26
	s_add_i32 m0, s16, 0x2000
	s_mov_b64 s[20:21], 0x2000
	v_lshl_add_u64 v[196:197], s[22:23], 0, v[0:1]
	global_load_lds_dwordx4 v0, s[22:23]
	v_lshl_add_u64 v[2:3], v[194:195], 0, s[20:21]
	s_add_i32 m0, s16, 0x4000
	v_and_b32_e32 v6, 19, v4
	global_load_lds_dwordx4 v[2:3], off
	v_lshl_add_u64 v[2:3], v[196:197], 0, s[20:21]
	s_add_i32 m0, s16, 0x6000
	v_lshlrev_b32_e32 v7, 1, v4
	global_load_lds_dwordx4 v[2:3], off
	v_lshrrev_b32_e32 v4, 1, v4
	v_lshlrev_b32_e32 v15, 10, v5
	v_and_b32_e32 v5, 8, v7
	v_and_b32_e32 v4, 4, v4
	v_or3_b32 v4, v6, v5, v4
	v_lshl_or_b32 v214, v4, 4, v15
	v_mov_b32_e32 v162, v1
	v_add_u32_e32 v215, 0, v214
	s_waitcnt vmcnt(0)
	s_waitcnt vmcnt(0) lgkmcnt(0)
	s_barrier
	ds_read_b128 v[2:5], v215
	ds_read_b128 v[98:101], v215 offset:512
	v_lshl_or_b32 v0, v14, 4, v15
	s_mov_b32 s17, 1
	s_mov_b32 s22, 0
	s_mov_b32 s19, 2
	s_mov_b32 s20, 0
	s_mov_b32 s21, 0
	v_add_u32_e32 v231, 0, v0
	v_mov_b32_e32 v163, v162
	v_mov_b32_e32 v164, v162
	v_mov_b32_e32 v165, v162
	v_mov_b32_e32 v166, v162
	v_mov_b32_e32 v167, v162
	v_mov_b32_e32 v168, v162
	v_mov_b32_e32 v169, v162
	s_waitcnt lgkmcnt(1)
	v_mfma_f32_32x32x16_bf16 v[82:97], v[2:5], v[130:133], 0
	v_mov_b32_e32 v174, v162
	v_mov_b32_e32 v175, v162
	v_mov_b32_e32 v176, v162
	v_mov_b32_e32 v177, v162
	v_mov_b32_e32 v170, v162
	v_mov_b32_e32 v171, v162
	v_mov_b32_e32 v172, v162
	v_mfma_f32_32x32x16_bf16 v[66:81], v[2:5], v[134:137], 0
	ds_read_b128 v[2:5], v215 offset:2048
	ds_read_b128 v[178:181], v215 offset:2560
	ds_read_b128 v[6:9], v215 offset:4096
	ds_read_b128 v[10:13], v215 offset:6144
	v_mov_b32_e32 v173, v162
	s_waitcnt lgkmcnt(3)
	v_mfma_f32_32x32x16_bf16 v[82:97], v[2:5], v[138:141], v[82:97]
	v_mfma_f32_32x32x16_bf16 v[66:81], v[2:5], v[142:145], v[66:81]
	v_mov_b32_e32 v2, 0
	v_mov_b32_e32 v3, v2
	v_mov_b32_e32 v4, v2
	v_mov_b32_e32 v5, v2
	v_mov_b32_e32 v14, v2
	v_mov_b32_e32 v15, v2
	v_mov_b32_e32 v16, v2
	s_waitcnt lgkmcnt(1)
	v_mfma_f32_32x32x16_bf16 v[82:97], v[6:9], v[146:149], v[82:97]
	v_mov_b32_e32 v17, v2
	v_mov_b32_e32 v18, v2
	v_mov_b32_e32 v19, v2
	v_mov_b32_e32 v20, v2
	v_mov_b32_e32 v21, v2
	v_mov_b32_e32 v22, v2
	v_mov_b32_e32 v23, v2
	v_mfma_f32_32x32x16_bf16 v[66:81], v[6:9], v[150:153], v[66:81]
	v_mov_b32_e32 v6, v2
	v_mov_b32_e32 v7, v2
	v_mov_b32_e32 v8, v2
	v_mov_b32_e32 v9, v2
	v_mov_b32_e32 v24, v2
	v_mov_b32_e32 v25, v2
	v_mov_b32_e32 v26, v2
	s_waitcnt lgkmcnt(0)
	v_mfma_f32_32x32x16_bf16 v[82:97], v[10:13], v[154:157], v[82:97]
	v_mov_b32_e32 v27, v2
	v_mov_b32_e32 v28, v2
	v_mov_b32_e32 v29, v2
	v_mov_b32_e32 v30, v2
	v_mov_b32_e32 v31, v2
	v_mov_b32_e32 v32, v2
	v_mov_b32_e32 v33, v2
	v_mfma_f32_32x32x16_bf16 v[66:81], v[10:13], v[158:161], v[66:81]
	v_mov_b32_e32 v10, v2
	v_mov_b32_e32 v11, v2
	v_mov_b32_e32 v12, v2
	v_mov_b32_e32 v13, v2
	v_mov_b32_e32 v50, v2
	v_mov_b32_e32 v51, v2
	v_mov_b32_e32 v52, v2
	v_mov_b32_e32 v53, v2
	v_mov_b32_e32 v54, v2
	v_mov_b32_e32 v55, v2
	v_mov_b32_e32 v56, v2
	v_mov_b32_e32 v57, v2
	v_mov_b32_e32 v58, v2
	v_mov_b32_e32 v59, v2
	v_mov_b32_e32 v60, v2
	v_mov_b32_e32 v61, v2
	v_mov_b32_e32 v62, v2
	v_mov_b32_e32 v63, v2
	v_mov_b32_e32 v64, v2
	v_mov_b32_e32 v65, v2
	v_mov_b32_e32 v34, v2
	v_mov_b32_e32 v35, v2
	v_mov_b32_e32 v36, v2
	v_mov_b32_e32 v37, v2
	v_mov_b32_e32 v38, v2
	v_mov_b32_e32 v39, v2
	v_mov_b32_e32 v40, v2
	v_mov_b32_e32 v41, v2
	v_mov_b32_e32 v42, v2
	v_mov_b32_e32 v43, v2
	v_mov_b32_e32 v44, v2
	v_mov_b32_e32 v45, v2
	v_mov_b32_e32 v46, v2
	v_mov_b32_e32 v47, v2
	v_mov_b32_e32 v48, v2
	v_mov_b32_e32 v49, v2
	v_mov_b32_e32 v186, v2
	v_mov_b32_e32 v187, v2
	v_mov_b32_e32 v233, v186
	v_mov_b32_e32 v227, v187
.LBB0_967:
	s_min_i32 s23, s21, 0x101
	s_lshl_b32 s23, s23, 13
	s_add_i32 s88, s23, 0x4000
	s_lshl_b32 s23, s19, 14
	s_add_i32 s23, s16, s23
	v_lshl_add_u64 v[102:103], v[194:195], 0, s[88:89]
	s_mov_b32 m0, s23
	v_lshl_add_u32 v211, s17, 14, v215
	global_load_lds_dwordx4 v[102:103], off
	v_lshl_add_u64 v[102:103], v[196:197], 0, s[88:89]
	s_add_i32 m0, s23, 0x2000
	s_lshl_b32 s23, s20, 14
	global_load_lds_dwordx4 v[102:103], off
	s_add_i32 s23, s23, 0
	v_add_u32_e32 v183, s23, v214
	ds_read_b128 v[188:191], v183 offset:4608
	v_add_u32_e32 v232, s23, v0
	v_lshl_add_u32 v192, s22, 14, v231
	v_exp_f32_e32 v216, v82
	v_exp_f32_e32 v218, v83
	v_mfma_f32_32x32x16_bf16 v[114:129], v[98:101], v[130:133], 0
	v_mfma_f32_32x32x16_bf16 v[98:113], v[98:101], v[134:137], 0
	v_cvt_pk_bf16_f32 v182, v216, v218
	v_add_f32_e32 v233, v216, v233
	v_add_f32_e32 v233, v218, v233
	v_exp_f32_e32 v220, v84
	v_exp_f32_e32 v222, v85
	ds_read_b128 v[82:85], v183 offset:6656
	v_cvt_pk_bf16_f32 v183, v220, v222
	v_add_f32_e32 v233, v220, v233
	v_add_f32_e32 v233, v222, v233
	v_exp_f32_e32 v224, v86
	v_exp_f32_e32 v238, v87
	v_mfma_f32_32x32x16_bf16 v[114:129], v[178:181], v[138:141], v[114:129]
	v_mfma_f32_32x32x16_bf16 v[98:113], v[178:181], v[142:145], v[98:113]
	v_cvt_pk_bf16_f32 v184, v224, v238
	v_add_f32_e32 v233, v224, v233
	v_add_f32_e32 v233, v238, v233
	v_exp_f32_e32 v240, v88
	v_exp_f32_e32 v242, v89
	ds_read_b128 v[86:89], v192 offset:12288
	v_cvt_pk_bf16_f32 v185, v240, v242
	v_add_f32_e32 v233, v240, v233
	v_add_f32_e32 v233, v242, v233
	v_exp_f32_e32 v244, v90
	v_exp_f32_e32 v246, v91
	s_waitcnt lgkmcnt(0)
	v_mfma_f32_32x32x16_bf16 v[114:129], v[188:191], v[146:149], v[114:129]
	v_mfma_f32_32x32x16_bf16 v[98:113], v[188:191], v[150:153], v[98:113]
	ds_read_b128 v[234:237], v192 offset:12800
	v_cvt_pk_bf16_f32 v178, v244, v246
	v_add_f32_e32 v233, v244, v233
	v_add_f32_e32 v233, v246, v233
	v_exp_f32_e32 v200, v92
	v_exp_f32_e32 v198, v93
	s_nop 0
	v_cvt_pk_bf16_f32 v179, v200, v198
	v_add_f32_e32 v233, v200, v233
	v_add_f32_e32 v233, v198, v233
	v_exp_f32_e32 v204, v94
	v_exp_f32_e32 v202, v95
	v_mfma_f32_32x32x16_bf16 v[114:129], v[82:85], v[154:157], v[114:129]
	v_mfma_f32_32x32x16_bf16 v[98:113], v[82:85], v[158:161], v[98:113]
	v_cvt_pk_bf16_f32 v180, v204, v202
	v_add_f32_e32 v233, v204, v233
	v_add_f32_e32 v233, v202, v233
	v_exp_f32_e32 v208, v96
	v_exp_f32_e32 v206, v97
	v_mfma_f32_32x32x16_bf16 v[2:17], v[86:89], v[162:165], v[2:17]
	ds_read_b128 v[82:85], v192 offset:14336
	v_cvt_pk_bf16_f32 v181, v208, v206
	v_add_f32_e32 v233, v208, v233
	v_add_f32_e32 v233, v206, v233
	v_exp_f32_e32 v217, v66
	v_exp_f32_e32 v219, v67
	s_waitcnt lgkmcnt(0)
	v_mfma_f32_32x32x16_bf16 v[18:33], v[234:237], v[162:165], v[18:33]
	ds_read_b128 v[90:93], v192 offset:14848
	v_cvt_pk_bf16_f32 v190, v217, v219
	v_add_f32_e32 v227, v217, v227
	v_add_f32_e32 v227, v219, v227
	v_exp_f32_e32 v221, v68
	v_exp_f32_e32 v223, v69
	v_mfma_f32_32x32x16_bf16 v[34:49], v[86:89], v[174:177], v[34:49]
	v_cvt_pk_bf16_f32 v191, v221, v223
	v_add_f32_e32 v227, v221, v227
	v_add_f32_e32 v227, v223, v227
	v_exp_f32_e32 v225, v70
	v_exp_f32_e32 v239, v71
	v_mfma_f32_32x32x16_bf16 v[50:65], v[234:237], v[174:177], v[50:65]
	v_cvt_pk_bf16_f32 v192, v225, v239
	v_add_f32_e32 v227, v225, v227
	v_add_f32_e32 v227, v239, v227
	v_exp_f32_e32 v241, v72
	v_exp_f32_e32 v243, v73
	v_mfma_f32_32x32x16_bf16 v[2:17], v[82:85], v[166:169], v[2:17]
	ds_read_b128 v[66:69], v211
	v_cvt_pk_bf16_f32 v193, v241, v243
	v_add_f32_e32 v227, v241, v227
	v_add_f32_e32 v227, v243, v227
	v_exp_f32_e32 v245, v74
	v_exp_f32_e32 v247, v75
	s_waitcnt lgkmcnt(0)
	v_mfma_f32_32x32x16_bf16 v[18:33], v[90:93], v[166:169], v[18:33]
	v_cvt_pk_bf16_f32 v186, v245, v247
	v_add_f32_e32 v227, v245, v227
	v_add_f32_e32 v227, v247, v227
	v_exp_f32_e32 v201, v76
	v_exp_f32_e32 v199, v77
	v_mfma_f32_32x32x16_bf16 v[34:49], v[82:85], v[170:173], v[34:49]
	ds_read_b128 v[164:167], v211 offset:2048
	v_cvt_pk_bf16_f32 v187, v201, v199
	v_add_f32_e32 v227, v201, v227
	v_add_f32_e32 v227, v199, v227
	v_exp_f32_e32 v205, v78
	v_exp_f32_e32 v203, v79
	v_mfma_f32_32x32x16_bf16 v[50:65], v[90:93], v[170:173], v[50:65]
	v_exp_f32_e32 v209, v80
	v_exp_f32_e32 v207, v81
	v_cvt_pk_bf16_f32 v188, v205, v203
	v_add_f32_e32 v227, v205, v227
	v_add_f32_e32 v227, v203, v227
	v_cvt_pk_bf16_f32 v189, v209, v207
	v_add_f32_e32 v227, v209, v227
	v_add_f32_e32 v227, v207, v227
	v_mfma_f32_32x32x16_bf16 v[82:97], v[66:69], v[130:133], 0
	ds_read_b128 v[168:171], v211 offset:4096
	v_exp_f32_e32 v172, v114
	v_exp_f32_e32 v216, v115
	v_mfma_f32_32x32x16_bf16 v[66:81], v[66:69], v[134:137], 0
	v_cvt_pk_bf16_f32 v162, v172, v216
	v_add_f32_e32 v233, v172, v233
	v_add_f32_e32 v233, v216, v233
	v_exp_f32_e32 v218, v116
	v_exp_f32_e32 v220, v117
	s_waitcnt lgkmcnt(0)
	v_mfma_f32_32x32x16_bf16 v[82:97], v[164:167], v[138:141], v[82:97]
	ds_read_b128 v[114:117], v211 offset:6144
	v_cvt_pk_bf16_f32 v163, v218, v220
	v_add_f32_e32 v233, v218, v233
	v_add_f32_e32 v233, v220, v233
	v_exp_f32_e32 v222, v118
	v_exp_f32_e32 v224, v119
	v_mfma_f32_32x32x16_bf16 v[66:81], v[164:167], v[142:145], v[66:81]
	v_cvt_pk_bf16_f32 v164, v222, v224
	v_add_f32_e32 v233, v222, v233
	v_add_f32_e32 v233, v224, v233
	v_exp_f32_e32 v238, v120
	v_exp_f32_e32 v240, v121
	v_mfma_f32_32x32x16_bf16 v[82:97], v[168:171], v[146:149], v[82:97]
	ds_read_b128 v[118:121], v232 offset:8192
	v_cvt_pk_bf16_f32 v165, v238, v240
	v_add_f32_e32 v233, v238, v233
	v_add_f32_e32 v233, v240, v233
	v_exp_f32_e32 v242, v122
	v_exp_f32_e32 v244, v123
	v_mfma_f32_32x32x16_bf16 v[66:81], v[168:171], v[150:153], v[66:81]
	ds_read_b128 v[234:237], v232 offset:8704
	v_cvt_pk_bf16_f32 v166, v242, v244
	v_add_f32_e32 v233, v242, v233
	v_add_f32_e32 v233, v244, v233
	v_exp_f32_e32 v246, v124
	v_exp_f32_e32 v248, v125
	s_waitcnt lgkmcnt(0)
	v_mfma_f32_32x32x16_bf16 v[82:97], v[114:117], v[154:157], v[82:97]
	v_cvt_pk_bf16_f32 v167, v246, v248
	v_add_f32_e32 v233, v246, v233
	v_add_f32_e32 v233, v248, v233
	v_exp_f32_e32 v126, v126
	v_exp_f32_e32 v212, v127
	v_mfma_f32_32x32x16_bf16 v[66:81], v[114:117], v[158:161], v[66:81]
	v_cvt_pk_bf16_f32 v168, v126, v212
	v_add_f32_e32 v233, v126, v233
	v_add_f32_e32 v233, v212, v233
	v_exp_f32_e32 v128, v128
	v_exp_f32_e32 v210, v129
	v_mfma_f32_32x32x16_bf16 v[2:17], v[118:121], v[182:185], v[2:17]
	ds_read_b128 v[114:117], v232 offset:10240
	v_exp_f32_e32 v173, v98
	v_cvt_pk_bf16_f32 v169, v128, v210
	v_add_f32_e32 v233, v128, v233
	v_add_f32_e32 v233, v210, v233
	v_exp_f32_e32 v217, v99
	v_mfma_f32_32x32x16_bf16 v[18:33], v[234:237], v[182:185], v[18:33]
	ds_read_b128 v[122:125], v232 offset:10752
	v_cvt_pk_bf16_f32 v174, v173, v217
	v_add_f32_e32 v227, v173, v227
	v_add_f32_e32 v227, v217, v227
	v_exp_f32_e32 v219, v100
	v_exp_f32_e32 v221, v101
	v_mfma_f32_32x32x16_bf16 v[34:49], v[118:121], v[190:193], v[34:49]
	v_cvt_pk_bf16_f32 v175, v219, v221
	v_add_f32_e32 v227, v219, v227
	v_add_f32_e32 v227, v221, v227
	v_exp_f32_e32 v223, v102
	v_exp_f32_e32 v225, v103
	v_mfma_f32_32x32x16_bf16 v[50:65], v[234:237], v[190:193], v[50:65]
	v_cvt_pk_bf16_f32 v176, v223, v225
	v_add_f32_e32 v227, v223, v227
	v_add_f32_e32 v227, v225, v227
	v_exp_f32_e32 v239, v104
	v_exp_f32_e32 v241, v105
	s_waitcnt lgkmcnt(0)
	v_mfma_f32_32x32x16_bf16 v[2:17], v[114:117], v[178:181], v[2:17]
	ds_read_b128 v[98:101], v211 offset:512
	v_cvt_pk_bf16_f32 v177, v239, v241
	v_add_f32_e32 v227, v239, v227
	v_add_f32_e32 v227, v241, v227
	v_exp_f32_e32 v243, v106
	v_exp_f32_e32 v245, v107
	v_mfma_f32_32x32x16_bf16 v[18:33], v[122:125], v[178:181], v[18:33]
	v_cvt_pk_bf16_f32 v170, v243, v245
	v_add_f32_e32 v227, v243, v227
	v_add_f32_e32 v227, v245, v227
	v_exp_f32_e32 v247, v108
	v_exp_f32_e32 v249, v109
	v_mfma_f32_32x32x16_bf16 v[34:49], v[114:117], v[186:189], v[34:49]
	ds_read_b128 v[178:181], v211 offset:2560
	v_cvt_pk_bf16_f32 v171, v247, v249
	v_add_f32_e32 v227, v247, v227
	v_add_f32_e32 v227, v249, v227
	v_exp_f32_e32 v127, v110
	v_exp_f32_e32 v213, v111
	v_mfma_f32_32x32x16_bf16 v[50:65], v[122:125], v[186:189], v[50:65]
	v_exp_f32_e32 v129, v112
	v_exp_f32_e32 v211, v113
	v_cvt_pk_bf16_f32 v172, v127, v213
	v_add_f32_e32 v227, v127, v227
	v_add_f32_e32 v227, v213, v227
	v_cvt_pk_bf16_f32 v173, v129, v211
	v_add_f32_e32 v227, v129, v227
	v_add_f32_e32 v227, v211, v227
	s_add_i32 s22, s19, 1
	s_waitcnt vmcnt(0)
	s_and_b32 s23, s22, 3
	s_add_i32 s21, s21, 1
	s_cmpk_eq_i32 s21, 0x104
	s_mov_b32 s22, s20
	s_mov_b32 s20, s17
	s_mov_b32 s17, s19
	s_mov_b32 s19, s23
	s_waitcnt vmcnt(0) lgkmcnt(0)
	s_barrier
	s_cbranch_scc0 .LBB0_967
	v_mov_b32_e32 v186, v233
	v_mov_b32_e32 v187, v227
	v_mov_b32_e32 v227, 0x7c
	ds_read_b128 v[66:69], v232 offset:12288
	ds_read_b128 v[70:73], v232 offset:12800
	v_mov_b32_e32 v0, v230
	s_waitcnt lgkmcnt(1)
	v_mfma_f32_32x32x16_bf16 v[2:17], v[66:69], v[162:165], v[2:17]
	s_waitcnt lgkmcnt(0)
	v_mfma_f32_32x32x16_bf16 v[18:33], v[70:73], v[162:165], v[18:33]
	v_mfma_f32_32x32x16_bf16 v[34:49], v[66:69], v[174:177], v[34:49]
	v_mfma_f32_32x32x16_bf16 v[50:65], v[70:73], v[174:177], v[50:65]
	ds_read_b128 v[66:69], v232 offset:14336
	ds_read_b128 v[70:73], v232 offset:14848
	s_nop 0
	v_readfirstlane_b32 s16, v0
	s_ashr_i32 s16, s16, 1
	s_andn2_b32 s16, s16, 31
	s_cmpk_lt_i32 s16, 0x100
	s_waitcnt lgkmcnt(1)
	v_mfma_f32_32x32x16_bf16 v[2:17], v[66:69], v[166:169], v[2:17]
	s_waitcnt lgkmcnt(0)
	v_mfma_f32_32x32x16_bf16 v[18:33], v[70:73], v[166:169], v[18:33]
	v_mfma_f32_32x32x16_bf16 v[34:49], v[66:69], v[170:173], v[34:49]
	v_mbcnt_lo_u32_b32 v66, -1, 0
	v_mbcnt_hi_u32_b32 v66, -1, v66
	v_mbcnt_lo_u32_b32 v67, -1, 0
	v_mbcnt_hi_u32_b32 v67, -1, v67
	s_nop 0
	v_lshlrev_b32_e32 v66, 2, v66
	v_lshlrev_b32_e32 v67, 2, v67
	v_xor_b32_e32 v66, 0x80, v66
	v_xor_b32_e32 v67, 0x80, v67
	v_mfma_f32_32x32x16_bf16 v[50:65], v[70:73], v[170:173], v[50:65]
	ds_bpermute_b32 v66, v66, v186
	ds_bpermute_b32 v67, v67, v187
	s_cbranch_scc0 .LBB0_965
	s_lshl_b64 s[6:7], s[6:7], 11
	s_waitcnt lgkmcnt(1)
	v_add_f32_e32 v66, v186, v66
	s_add_u32 s6, s2, s6
	v_rcp_f32_e32 v66, v66
	s_addc_u32 s7, s3, s7
	s_lshl_b32 s15, s15, 1
	v_and_or_b32 v68, v0, 31, s16
	s_add_u32 s6, s6, s15
	v_ashrrev_i32_e32 v69, 31, v68
	s_addc_u32 s7, s7, 0
	s_waitcnt lgkmcnt(0)
	v_add_f32_e32 v67, v187, v67
	v_lshlrev_b64 v[68:69], 11, v[68:69]
	v_lshrrev_b32_e32 v0, 2, v0
	v_rcp_f32_e32 v70, v67
	v_lshl_add_u64 v[68:69], s[6:7], 0, v[68:69]
	v_pk_mul_f32 v[2:3], v[2:3], v[66:67] op_sel_hi:[1,0]
	v_pk_mul_f32 v[4:5], v[4:5], v[66:67] op_sel_hi:[1,0]
	v_and_b32_e32 v0, 8, v0
	v_pk_mul_f32 v[18:19], v[18:19], v[66:67] op_sel_hi:[1,0]
	v_pk_mul_f32 v[20:21], v[20:21], v[66:67] op_sel_hi:[1,0]
	v_pk_mul_f32 v[22:23], v[22:23], v[66:67] op_sel_hi:[1,0]
	v_pk_mul_f32 v[24:25], v[24:25], v[66:67] op_sel_hi:[1,0]
	v_pk_mul_f32 v[26:27], v[26:27], v[66:67] op_sel_hi:[1,0]
	v_pk_mul_f32 v[28:29], v[28:29], v[66:67] op_sel_hi:[1,0]
	v_pk_mul_f32 v[30:31], v[30:31], v[66:67] op_sel_hi:[1,0]
	v_pk_mul_f32 v[32:33], v[32:33], v[66:67] op_sel_hi:[1,0]
	v_pk_mul_f32 v[6:7], v[6:7], v[66:67] op_sel_hi:[1,0]
	v_pk_mul_f32 v[8:9], v[8:9], v[66:67] op_sel_hi:[1,0]
	v_pk_mul_f32 v[10:11], v[10:11], v[66:67] op_sel_hi:[1,0]
	v_pk_mul_f32 v[12:13], v[12:13], v[66:67] op_sel_hi:[1,0]
	v_pk_mul_f32 v[14:15], v[14:15], v[66:67] op_sel_hi:[1,0]
	v_pk_mul_f32 v[16:17], v[16:17], v[66:67] op_sel_hi:[1,0]
	v_lshl_add_u64 v[66:67], v[68:69], 0, v[0:1]
	v_cvt_pk_bf16_f32 v2, v2, v3
	v_cvt_pk_bf16_f32 v3, v4, v5
	v_cvt_pk_bf16_f32 v4, v18, v19
	v_cvt_pk_bf16_f32 v5, v20, v21
	global_store_dwordx2 v[66:67], v[2:3], off offset:1536
	global_store_dwordx2 v[66:67], v[4:5], off offset:1600
	v_cvt_pk_bf16_f32 v2, v6, v7
	v_cvt_pk_bf16_f32 v3, v8, v9
	v_cvt_pk_bf16_f32 v4, v22, v23
	v_cvt_pk_bf16_f32 v5, v24, v25
	global_store_dwordx2 v[66:67], v[2:3], off offset:1552
	global_store_dwordx2 v[66:67], v[4:5], off offset:1616
	v_cvt_pk_bf16_f32 v2, v10, v11
	v_cvt_pk_bf16_f32 v3, v12, v13
	v_pk_mul_f32 v[34:35], v[34:35], v[70:71] op_sel_hi:[1,0]
	v_pk_mul_f32 v[36:37], v[36:37], v[70:71] op_sel_hi:[1,0]
	v_cvt_pk_bf16_f32 v4, v26, v27
	v_cvt_pk_bf16_f32 v5, v28, v29
	global_store_dwordx2 v[66:67], v[2:3], off offset:1568
	global_store_dwordx2 v[66:67], v[4:5], off offset:1632
	v_cvt_pk_bf16_f32 v2, v14, v15
	v_cvt_pk_bf16_f32 v3, v16, v17
	v_pk_mul_f32 v[50:51], v[50:51], v[70:71] op_sel_hi:[1,0]
	v_pk_mul_f32 v[52:53], v[52:53], v[70:71] op_sel_hi:[1,0]
	v_pk_mul_f32 v[38:39], v[38:39], v[70:71] op_sel_hi:[1,0]
	v_pk_mul_f32 v[40:41], v[40:41], v[70:71] op_sel_hi:[1,0]
	v_cvt_pk_bf16_f32 v4, v30, v31
	v_cvt_pk_bf16_f32 v5, v32, v33
	global_store_dwordx2 v[66:67], v[2:3], off offset:1584
	global_store_dwordx2 v[66:67], v[4:5], off offset:1648
	v_cvt_pk_bf16_f32 v2, v34, v35
	v_cvt_pk_bf16_f32 v3, v36, v37
	v_pk_mul_f32 v[54:55], v[54:55], v[70:71] op_sel_hi:[1,0]
	v_pk_mul_f32 v[56:57], v[56:57], v[70:71] op_sel_hi:[1,0]
	v_pk_mul_f32 v[42:43], v[42:43], v[70:71] op_sel_hi:[1,0]
	v_pk_mul_f32 v[44:45], v[44:45], v[70:71] op_sel_hi:[1,0]
	v_cvt_pk_bf16_f32 v4, v50, v51
	v_cvt_pk_bf16_f32 v5, v52, v53
	global_store_dwordx2 v[66:67], v[2:3], off offset:1664
	global_store_dwordx2 v[66:67], v[4:5], off offset:1728
	v_cvt_pk_bf16_f32 v2, v38, v39
	v_cvt_pk_bf16_f32 v3, v40, v41
	v_pk_mul_f32 v[58:59], v[58:59], v[70:71] op_sel_hi:[1,0]
	v_pk_mul_f32 v[60:61], v[60:61], v[70:71] op_sel_hi:[1,0]
	v_pk_mul_f32 v[46:47], v[46:47], v[70:71] op_sel_hi:[1,0]
	v_pk_mul_f32 v[48:49], v[48:49], v[70:71] op_sel_hi:[1,0]
	v_cvt_pk_bf16_f32 v4, v54, v55
	v_cvt_pk_bf16_f32 v5, v56, v57
	global_store_dwordx2 v[66:67], v[2:3], off offset:1680
	global_store_dwordx2 v[66:67], v[4:5], off offset:1744
	v_cvt_pk_bf16_f32 v2, v42, v43
	v_cvt_pk_bf16_f32 v3, v44, v45
	v_pk_mul_f32 v[62:63], v[62:63], v[70:71] op_sel_hi:[1,0]
	v_pk_mul_f32 v[64:65], v[64:65], v[70:71] op_sel_hi:[1,0]
	v_cvt_pk_bf16_f32 v4, v58, v59
	v_cvt_pk_bf16_f32 v5, v60, v61
	global_store_dwordx2 v[66:67], v[2:3], off offset:1696
	global_store_dwordx2 v[66:67], v[4:5], off offset:1760
	v_cvt_pk_bf16_f32 v2, v46, v47
	v_cvt_pk_bf16_f32 v3, v48, v49
	v_cvt_pk_bf16_f32 v4, v62, v63
	v_cvt_pk_bf16_f32 v5, v64, v65
	global_store_dwordx2 v[66:67], v[2:3], off offset:1712
	global_store_dwordx2 v[66:67], v[4:5], off offset:1776
	s_branch .LBB0_965
